# v49 + P3 and P8 epilogues software-pipelined by one stage (operand loads of the next 16-row block issued before the current block's compute, own pointers, rotating register sets, vmcnt recomputed)
# speedup vs baseline: 1.0093x; 1.0074x over previous
; #define G_ENDTILE(VM) do { asm volatile("s_waitcnt vmcnt(" #VM ")" ::: "memory"); \
;         asm volatile("s_waitcnt lgkmcnt(0)" ::: "memory"); __builtin_amdgcn_s_barrier(); asm volatile("" ::: "memory"); } while (0)
;     ...
;         for (int t = 0; t < nt - 2; t += 2) {
;             G_TILE(G_A0, G_B0, true, G_B1, G_A1, t + 1, true, t + 2, (void)0);
;             G_ENDTILE(8);
;             G_TILE(G_A1, G_B1, true, G_B0, G_A0, t + 2, true, t + 3, (void)0);
;             G_ENDTILE(8);
.LBB0_375:
	s_mov_b32 m0, s72
	ds_read_b64_tr_b16 v[170:171], v165
	ds_read_b64_tr_b16 v[174:175], v165 offset:32
	ds_read_b64_tr_b16 v[178:179], v165 offset:64
	ds_read_b64_tr_b16 v[182:183], v165 offset:96
	ds_read_b64_tr_b16 v[172:173], v166
	ds_read_b64_tr_b16 v[176:177], v166 offset:32
	ds_read_b64_tr_b16 v[180:181], v166 offset:64
	ds_read_b64_tr_b16 v[184:185], v166 offset:96
	ds_read_b128 v[186:189], v162
	ds_read_b128 v[190:193], v162 offset:2048
	ds_read_b128 v[198:201], v162 offset:4096
	buffer_load_dwordx4 v163, s[20:23], s73 offen lds
	s_mov_b32 m0, s71
	s_and_b32 s17, s53, 0xffff
	buffer_load_dwordx4 v164, s[20:23], s73 offen lds
	s_mov_b32 m0, s70
	s_and_b32 s13, s48, 0xffff
	buffer_load_dwordx4 v167, s[20:23], s73 offen lds
	s_mov_b32 m0, s68
	s_mov_b32 s12, s47
	buffer_load_dwordx4 v168, s[20:23], s73 offen lds
	v_mbcnt_lo_u32_b32 v163, -1, 0
	v_mbcnt_hi_u32_b32 v163, -1, v163
	s_mov_b32 s16, s49
	v_lshlrev_b32_e32 v164, 4, v163
	v_and_b32_e32 v167, 32, v163
	v_lshrrev_b32_e32 v163, 2, v163
	v_bitop3_b32 v164, v164, v167, 48 bitop3:0x6c
	v_add_lshl_u32 v163, v163, s54, 12
	v_or3_b32 v163, v164, s55, v163
	s_mov_b32 s20, s49
	s_mov_b32 s21, s17
	s_mov_b32 s22, s10
	s_mov_b32 s23, s11
	s_and_b32 s19, s46, 0xffff
	s_mov_b32 s18, s43
	v_add_u32_e32 v164, 0x40000, v163
	v_add_u32_e32 v167, 0x80000, v163
	v_add_u32_e32 v168, 0xc0000, v163
	s_mov_b32 s8, s47
	s_mov_b32 s9, s13
	s_mov_b32 s24, s43
	s_mov_b32 s25, s19
	s_mov_b32 s26, s10
	s_mov_b32 s27, s11
	s_waitcnt lgkmcnt(2)
	v_mfma_f32_16x16x32_bf16 v[156:159], v[170:173], v[186:189], v[156:159]
	v_mfma_f32_16x16x32_bf16 v[152:155], v[174:177], v[186:189], v[152:155]
	v_mfma_f32_16x16x32_bf16 v[148:151], v[178:181], v[186:189], v[148:151]
	v_mfma_f32_16x16x32_bf16 v[144:147], v[182:185], v[186:189], v[144:147]
	s_waitcnt vmcnt(11)
	v_cvt_pk_bf16_f32 v15, v14, v15
	v_cvt_pk_bf16_f32 v14, v12, v13
	ds_read_b128 v[186:189], v162 offset:6144
	ds_write_b64 v161, v[14:15] offset:34816
	s_waitcnt lgkmcnt(3)
	v_mfma_f32_16x16x32_bf16 v[12:15], v[182:185], v[190:193], v[128:131]
	v_mfma_f32_16x16x32_bf16 v[140:143], v[170:173], v[190:193], v[140:143]
	v_mfma_f32_16x16x32_bf16 v[136:139], v[174:177], v[190:193], v[136:139]
	v_mfma_f32_16x16x32_bf16 v[132:135], v[178:181], v[190:193], v[132:135]
	buffer_load_dwordx4 v[128:131], v160, s[8:11], 0 offen
	ds_read_b128 v[190:193], v162 offset:8192
	s_waitcnt lgkmcnt(3)
	v_mfma_f32_16x16x32_bf16 v[124:127], v[170:173], v[198:201], v[124:127]
	v_mfma_f32_16x16x32_bf16 v[120:123], v[174:177], v[198:201], v[120:123]
	v_mfma_f32_16x16x32_bf16 v[116:119], v[178:181], v[198:201], v[116:119]
	v_mfma_f32_16x16x32_bf16 v[112:115], v[182:185], v[198:201], v[112:115]
	s_waitcnt vmcnt(10)
	v_cvt_pk_bf16_f32 v31, v30, v31
	v_cvt_pk_bf16_f32 v30, v28, v29
	ds_read_b128 v[198:201], v162 offset:10240
	ds_write_b64 v161, v[30:31] offset:43520
	s_waitcnt lgkmcnt(4)
	v_mfma_f32_16x16x32_bf16 v[28:31], v[182:185], v[186:189], v[96:99]
	v_mfma_f32_16x16x32_bf16 v[108:111], v[170:173], v[186:189], v[108:111]
	v_mfma_f32_16x16x32_bf16 v[104:107], v[174:177], v[186:189], v[104:107]
	v_mfma_f32_16x16x32_bf16 v[100:103], v[178:181], v[186:189], v[100:103]
	buffer_load_dwordx4 v[96:99], v160, s[8:11], s11 offen
	ds_read_b128 v[186:189], v162 offset:12288
	s_waitcnt lgkmcnt(3)
	v_mfma_f32_16x16x32_bf16 v[92:95], v[170:173], v[190:193], v[92:95]
	v_mfma_f32_16x16x32_bf16 v[88:91], v[174:177], v[190:193], v[88:91]
	v_mfma_f32_16x16x32_bf16 v[84:87], v[178:181], v[190:193], v[84:87]
	v_mfma_f32_16x16x32_bf16 v[80:83], v[182:185], v[190:193], v[80:83]
	v_cvt_pk_bf16_f32 v7, v6, v7
	v_cvt_pk_bf16_f32 v6, v4, v5
	ds_read_b128 v[190:193], v162 offset:14336
	ds_write_b64 v161, v[6:7] offset:52224
	s_waitcnt lgkmcnt(4)
	v_mfma_f32_16x16x32_bf16 v[4:7], v[182:185], v[198:201], v[64:67]
	v_mfma_f32_16x16x32_bf16 v[76:79], v[170:173], v[198:201], v[76:79]
	v_mfma_f32_16x16x32_bf16 v[72:75], v[174:177], v[198:201], v[72:75]
	v_mfma_f32_16x16x32_bf16 v[68:71], v[178:181], v[198:201], v[68:71]
	buffer_load_dwordx4 v[64:67], v160, s[8:11], s56 offen
	ds_read_b128 v[198:201], v162 offset:1024
	s_waitcnt lgkmcnt(3)
	v_mfma_f32_16x16x32_bf16 v[60:63], v[170:173], v[186:189], v[60:63]
	v_mfma_f32_16x16x32_bf16 v[56:59], v[174:177], v[186:189], v[56:59]
	v_mfma_f32_16x16x32_bf16 v[52:55], v[178:181], v[186:189], v[52:55]
	v_mfma_f32_16x16x32_bf16 v[48:51], v[182:185], v[186:189], v[48:51]
	s_waitcnt lgkmcnt(2)
	v_mfma_f32_16x16x32_bf16 v[44:47], v[170:173], v[190:193], v[44:47]
	ds_read_b128 v[170:173], v162 offset:3072
	v_mfma_f32_16x16x32_bf16 v[40:43], v[174:177], v[190:193], v[40:43]
	ds_read_b64_tr_b16 v[174:175], v165 offset:17408
	ds_read_b64_tr_b16 v[186:187], v165 offset:17440
	ds_read_b64_tr_b16 v[202:203], v165 offset:17472
	ds_read_b64_tr_b16 v[206:207], v165 offset:17504
	ds_read_b64_tr_b16 v[176:177], v166 offset:17408
	ds_read_b64_tr_b16 v[188:189], v166 offset:17440
	ds_read_b64_tr_b16 v[204:205], v166 offset:17472
	ds_read_b64_tr_b16 v[208:209], v166 offset:17504
	v_mfma_f32_16x16x32_bf16 v[36:39], v[178:181], v[190:193], v[36:39]
	s_waitcnt vmcnt(11)
	v_cvt_pk_bf16_f32 v179, v26, v27
	v_cvt_pk_bf16_f32 v178, v24, v25
	ds_write_b64 v161, v[178:179] offset:60928
	v_mfma_f32_16x16x32_bf16 v[24:27], v[182:185], v[190:193], v[32:35]
	s_nop 2
	buffer_load_dwordx4 v[32:35], v160, s[8:11], s57 offen
	ds_read_b128 v[178:181], v162 offset:5120
	s_waitcnt lgkmcnt(5)
	v_mfma_f32_16x16x32_bf16 v[156:159], v[174:177], v[198:201], v[156:159]
	s_waitcnt lgkmcnt(4)
	v_mfma_f32_16x16x32_bf16 v[152:155], v[186:189], v[198:201], v[152:155]
	s_waitcnt lgkmcnt(3)
	v_mfma_f32_16x16x32_bf16 v[148:151], v[202:205], v[198:201], v[148:151]
	s_waitcnt lgkmcnt(2)
	v_mfma_f32_16x16x32_bf16 v[144:147], v[206:209], v[198:201], v[144:147]
	ds_read_b128 v[182:185], v162 offset:7168
	v_mfma_f32_16x16x32_bf16 v[12:15], v[206:209], v[170:173], v[12:15]
	s_waitcnt vmcnt(11)
	v_cvt_pk_bf16_f32 v23, v22, v23
	v_cvt_pk_bf16_f32 v22, v20, v21
	ds_write_b64 v161, v[22:23] offset:35072
	v_mfma_f32_16x16x32_bf16 v[140:143], v[174:177], v[170:173], v[140:143]
	v_mfma_f32_16x16x32_bf16 v[136:139], v[186:189], v[170:173], v[136:139]
	v_mfma_f32_16x16x32_bf16 v[132:135], v[202:205], v[170:173], v[132:135]
	buffer_load_dwordx4 v[20:23], v160, s[20:23], 0 offen
	ds_read_b128 v[170:173], v162 offset:9216
	s_waitcnt lgkmcnt(3)
	v_mfma_f32_16x16x32_bf16 v[124:127], v[174:177], v[178:181], v[124:127]
	v_mfma_f32_16x16x32_bf16 v[120:123], v[186:189], v[178:181], v[120:123]
	v_mfma_f32_16x16x32_bf16 v[116:119], v[202:205], v[178:181], v[116:119]
	v_mfma_f32_16x16x32_bf16 v[112:115], v[206:209], v[178:181], v[112:115]
	s_waitcnt vmcnt(10)
	v_cvt_pk_bf16_f32 v11, v10, v11
	v_cvt_pk_bf16_f32 v10, v8, v9
	ds_read_b128 v[178:181], v162 offset:11264
	ds_write_b64 v161, v[10:11] offset:43776
	s_waitcnt lgkmcnt(4)
	v_mfma_f32_16x16x32_bf16 v[8:11], v[206:209], v[182:185], v[28:31]
	v_mfma_f32_16x16x32_bf16 v[108:111], v[174:177], v[182:185], v[108:111]
	v_mfma_f32_16x16x32_bf16 v[104:107], v[186:189], v[182:185], v[104:107]
	v_mfma_f32_16x16x32_bf16 v[100:103], v[202:205], v[182:185], v[100:103]
	buffer_load_dwordx4 v[182:185], v160, s[20:23], s11 offen
	ds_read_b128 v[28:31], v162 offset:13312
	s_waitcnt lgkmcnt(3)
	v_mfma_f32_16x16x32_bf16 v[92:95], v[174:177], v[170:173], v[92:95]
	v_mfma_f32_16x16x32_bf16 v[88:91], v[186:189], v[170:173], v[88:91]
	v_mfma_f32_16x16x32_bf16 v[84:87], v[202:205], v[170:173], v[84:87]
	v_mfma_f32_16x16x32_bf16 v[80:83], v[206:209], v[170:173], v[80:83]
	v_cvt_pk_bf16_f32 v3, v2, v3
	v_cvt_pk_bf16_f32 v2, v0, v1
	ds_read_b128 v[170:173], v162 offset:15360
	ds_write_b64 v161, v[2:3] offset:52480
	s_waitcnt lgkmcnt(4)
	v_mfma_f32_16x16x32_bf16 v[0:3], v[206:209], v[178:181], v[4:7]
	v_mfma_f32_16x16x32_bf16 v[76:79], v[174:177], v[178:181], v[76:79]
	v_mfma_f32_16x16x32_bf16 v[72:75], v[186:189], v[178:181], v[72:75]
	v_mfma_f32_16x16x32_bf16 v[68:71], v[202:205], v[178:181], v[68:71]
	buffer_load_dwordx4 v[178:181], v160, s[20:23], s56 offen
	s_waitcnt lgkmcnt(2)
	v_mfma_f32_16x16x32_bf16 v[60:63], v[174:177], v[28:31], v[60:63]
	v_mfma_f32_16x16x32_bf16 v[56:59], v[186:189], v[28:31], v[56:59]
	v_mfma_f32_16x16x32_bf16 v[52:55], v[202:205], v[28:31], v[52:55]
	v_mfma_f32_16x16x32_bf16 v[48:51], v[206:209], v[28:31], v[48:51]
	s_waitcnt vmcnt(11)
	v_cvt_pk_bf16_f32 v5, v18, v19
	v_cvt_pk_bf16_f32 v4, v16, v17
	s_waitcnt lgkmcnt(1)
	v_mfma_f32_16x16x32_bf16 v[16:19], v[206:209], v[170:173], v[24:27]
	ds_write_b64 v161, v[4:5] offset:61184
	v_mfma_f32_16x16x32_bf16 v[44:47], v[174:177], v[170:173], v[44:47]
	v_mfma_f32_16x16x32_bf16 v[40:43], v[186:189], v[170:173], v[40:43]
	v_mfma_f32_16x16x32_bf16 v[36:39], v[202:205], v[170:173], v[36:39]
	buffer_load_dwordx4 v[170:173], v160, s[20:23], s57 offen
	s_waitcnt vmcnt(8)
	s_mov_b32 m0, s59
	s_waitcnt lgkmcnt(0)
	s_barrier
	ds_read_b64_tr_b16 v[24:25], v165 offset:34816
	ds_read_b64_tr_b16 v[26:27], v166 offset:34816
	ds_read_b64_tr_b16 v[176:177], v166 offset:34848
	ds_read_b128 v[4:7], v162 offset:32768
	ds_read_b64_tr_b16 v[174:175], v165 offset:34848
	ds_read_b64_tr_b16 v[186:187], v165 offset:34880
	ds_read_b64_tr_b16 v[190:191], v165 offset:34912
	ds_read_b64_tr_b16 v[188:189], v166 offset:34880
	ds_read_b64_tr_b16 v[192:193], v166 offset:34912
	ds_read_b128 v[28:31], v162 offset:34816
	ds_read_b128 v[198:201], v162 offset:36864
	buffer_load_dwordx4 v163, s[24:27], 0 offen lds
	s_mov_b32 m0, s60
	s_waitcnt lgkmcnt(7)
	v_mfma_f32_16x16x32_bf16 v[156:159], v[24:27], v[4:7], v[156:159]
	buffer_load_dwordx4 v164, s[24:27], 0 offen lds
	s_mov_b32 m0, s61
	s_nop 0
	buffer_load_dwordx4 v167, s[24:27], 0 offen lds
	s_mov_b32 m0, s62
	s_waitcnt lgkmcnt(6)
	v_mfma_f32_16x16x32_bf16 v[152:155], v[174:177], v[4:7], v[152:155]
	buffer_load_dwordx4 v168, s[24:27], 0 offen lds
	s_waitcnt lgkmcnt(3)
	v_mfma_f32_16x16x32_bf16 v[148:151], v[186:189], v[4:7], v[148:151]
	s_waitcnt lgkmcnt(2)
	v_mfma_f32_16x16x32_bf16 v[144:147], v[190:193], v[4:7], v[144:147]
	ds_read_b128 v[4:7], v162 offset:38912
	s_waitcnt vmcnt(11)
	v_cvt_pk_bf16_f32 v131, v130, v131
	v_cvt_pk_bf16_f32 v130, v128, v129
	s_waitcnt lgkmcnt(2)
	v_mfma_f32_16x16x32_bf16 v[140:143], v[24:27], v[28:31], v[140:143]
	ds_write_b64 v161, v[130:131]
	v_mfma_f32_16x16x32_bf16 v[202:205], v[174:177], v[28:31], v[136:139]
	v_mfma_f32_16x16x32_bf16 v[132:135], v[186:189], v[28:31], v[132:135]
	v_mfma_f32_16x16x32_bf16 v[206:209], v[190:193], v[28:31], v[12:15]
	s_nop 2
	buffer_load_dwordx4 v[12:15], v160, s[8:11], s63 offen
	ds_read_b128 v[128:131], v162 offset:40960
	s_waitcnt lgkmcnt(3)
	v_mfma_f32_16x16x32_bf16 v[124:127], v[24:27], v[198:201], v[124:127]
	v_mfma_f32_16x16x32_bf16 v[120:123], v[174:177], v[198:201], v[120:123]
	v_mfma_f32_16x16x32_bf16 v[116:119], v[186:189], v[198:201], v[116:119]
	v_mfma_f32_16x16x32_bf16 v[198:201], v[190:193], v[198:201], v[112:115]
	s_waitcnt lgkmcnt(2)
	v_mfma_f32_16x16x32_bf16 v[210:213], v[174:177], v[4:7], v[104:107]
	s_waitcnt vmcnt(11)
	v_cvt_pk_bf16_f32 v29, v98, v99
	v_cvt_pk_bf16_f32 v28, v96, v97
	ds_read_b128 v[104:107], v162 offset:43008
	v_mfma_f32_16x16x32_bf16 v[8:11], v[190:193], v[4:7], v[8:11]
	ds_write_b64 v161, v[28:29] offset:8704
	v_mfma_f32_16x16x32_bf16 v[108:111], v[24:27], v[4:7], v[108:111]
	v_mfma_f32_16x16x32_bf16 v[100:103], v[186:189], v[4:7], v[100:103]
	buffer_load_dwordx4 v[28:31], v160, s[8:11], s65 offen
	ds_read_b128 v[96:99], v162 offset:45056
	s_waitcnt lgkmcnt(3)
	v_mfma_f32_16x16x32_bf16 v[92:95], v[24:27], v[128:131], v[92:95]
	v_mfma_f32_16x16x32_bf16 v[88:91], v[174:177], v[128:131], v[88:91]
	v_mfma_f32_16x16x32_bf16 v[84:87], v[186:189], v[128:131], v[84:87]
	v_mfma_f32_16x16x32_bf16 v[214:217], v[190:193], v[128:131], v[80:83]
	s_waitcnt lgkmcnt(2)
	v_mfma_f32_16x16x32_bf16 v[218:221], v[174:177], v[104:107], v[72:75]
	s_waitcnt vmcnt(11)
	v_cvt_pk_bf16_f32 v5, v66, v67
	v_cvt_pk_bf16_f32 v4, v64, v65
	ds_read_b128 v[72:75], v162 offset:47104
	v_mfma_f32_16x16x32_bf16 v[0:3], v[190:193], v[104:107], v[0:3]
	ds_write_b64 v161, v[4:5] offset:17408
	v_mfma_f32_16x16x32_bf16 v[76:79], v[24:27], v[104:107], v[76:79]
	v_mfma_f32_16x16x32_bf16 v[68:71], v[186:189], v[104:107], v[68:71]
	buffer_load_dwordx4 v[4:7], v160, s[8:11], s64 offen
	ds_read_b128 v[64:67], v162 offset:33792
	s_waitcnt lgkmcnt(3)
	v_mfma_f32_16x16x32_bf16 v[60:63], v[24:27], v[96:99], v[60:63]
	v_mfma_f32_16x16x32_bf16 v[56:59], v[174:177], v[96:99], v[56:59]
	v_mfma_f32_16x16x32_bf16 v[52:55], v[186:189], v[96:99], v[52:55]
	v_mfma_f32_16x16x32_bf16 v[48:51], v[190:193], v[96:99], v[48:51]
	ds_read_b128 v[80:83], v162 offset:35840
	s_waitcnt lgkmcnt(3)
	v_mfma_f32_16x16x32_bf16 v[174:177], v[174:177], v[72:75], v[40:43]
	s_nop 2
	ds_read_b64_tr_b16 v[40:41], v165 offset:52224
	ds_read_b64_tr_b16 v[222:223], v165 offset:52256
	ds_read_b64_tr_b16 v[226:227], v165 offset:52288
	ds_read_b64_tr_b16 v[230:231], v165 offset:52320
	ds_read_b64_tr_b16 v[42:43], v166 offset:52224
	ds_read_b64_tr_b16 v[224:225], v166 offset:52256
	ds_read_b64_tr_b16 v[228:229], v166 offset:52288
	ds_read_b64_tr_b16 v[232:233], v166 offset:52320
	v_mfma_f32_16x16x32_bf16 v[16:19], v[190:193], v[72:75], v[16:19]
	v_mfma_f32_16x16x32_bf16 v[44:47], v[24:27], v[72:75], v[44:47]
	s_waitcnt vmcnt(11)
	v_cvt_pk_bf16_f32 v25, v34, v35
	v_cvt_pk_bf16_f32 v24, v32, v33
	ds_write_b64 v161, v[24:25] offset:26112
	v_mfma_f32_16x16x32_bf16 v[186:189], v[186:189], v[72:75], v[36:39]
	buffer_load_dwordx4 v[24:27], v160, s[8:11], s66 offen
	ds_read_b128 v[32:35], v162 offset:37888
	s_waitcnt lgkmcnt(5)
	v_mfma_f32_16x16x32_bf16 v[156:159], v[40:43], v[64:67], v[156:159]
	s_waitcnt lgkmcnt(4)
	v_mfma_f32_16x16x32_bf16 v[152:155], v[222:225], v[64:67], v[152:155]
	s_waitcnt lgkmcnt(3)
	v_mfma_f32_16x16x32_bf16 v[148:151], v[226:229], v[64:67], v[148:151]
	s_waitcnt lgkmcnt(2)
	v_mfma_f32_16x16x32_bf16 v[190:193], v[230:233], v[64:67], v[144:147]
	ds_read_b128 v[36:39], v162 offset:39936
	s_waitcnt vmcnt(11)
	v_cvt_pk_bf16_f32 v23, v22, v23
	v_cvt_pk_bf16_f32 v22, v20, v21
	v_mfma_f32_16x16x32_bf16 v[136:139], v[40:43], v[80:83], v[140:143]
	ds_write_b64 v161, v[22:23] offset:256
	v_mfma_f32_16x16x32_bf16 v[128:131], v[222:225], v[80:83], v[202:205]
	v_mfma_f32_16x16x32_bf16 v[132:135], v[226:229], v[80:83], v[132:135]
	v_mfma_f32_16x16x32_bf16 v[140:143], v[230:233], v[80:83], v[206:209]
	buffer_load_dwordx4 v[20:23], v160, s[20:23], s63 offen
	ds_read_b128 v[64:67], v162 offset:41984
	s_waitcnt lgkmcnt(3)
	v_mfma_f32_16x16x32_bf16 v[124:127], v[40:43], v[32:35], v[124:127]
	v_mfma_f32_16x16x32_bf16 v[120:123], v[222:225], v[32:35], v[120:123]
	v_mfma_f32_16x16x32_bf16 v[112:115], v[226:229], v[32:35], v[116:119]
	v_mfma_f32_16x16x32_bf16 v[116:119], v[230:233], v[32:35], v[198:201]
	ds_read_b128 v[32:35], v162 offset:44032
	s_waitcnt vmcnt(11)
	v_cvt_pk_bf16_f32 v73, v184, v185
	v_cvt_pk_bf16_f32 v72, v182, v183
	s_waitcnt lgkmcnt(3)
	v_mfma_f32_16x16x32_bf16 v[104:107], v[40:43], v[36:39], v[108:111]
	ds_write_b64 v161, v[72:73] offset:8960
	v_mfma_f32_16x16x32_bf16 v[96:99], v[222:225], v[36:39], v[210:213]
	v_mfma_f32_16x16x32_bf16 v[100:103], v[226:229], v[36:39], v[100:103]
	v_mfma_f32_16x16x32_bf16 v[108:111], v[230:233], v[36:39], v[8:11]
	s_nop 2
	buffer_load_dwordx4 v[8:11], v160, s[20:23], s65 offen
	ds_read_b128 v[36:39], v162 offset:46080
	s_waitcnt lgkmcnt(3)
	v_mfma_f32_16x16x32_bf16 v[92:95], v[40:43], v[64:67], v[92:95]
	v_mfma_f32_16x16x32_bf16 v[88:91], v[222:225], v[64:67], v[88:91]
	v_mfma_f32_16x16x32_bf16 v[80:83], v[226:229], v[64:67], v[84:87]
	v_mfma_f32_16x16x32_bf16 v[84:87], v[230:233], v[64:67], v[214:217]
	ds_read_b128 v[144:147], v162 offset:48128
	s_waitcnt lgkmcnt(3)
	v_mfma_f32_16x16x32_bf16 v[72:75], v[40:43], v[32:35], v[76:79]
	s_waitcnt vmcnt(11)
	s_nop 1
	v_cvt_pk_bf16_f32 v77, v180, v181
	v_cvt_pk_bf16_f32 v76, v178, v179
	v_mfma_f32_16x16x32_bf16 v[64:67], v[222:225], v[32:35], v[218:221]
	ds_write_b64 v161, v[76:77] offset:17664
	v_mfma_f32_16x16x32_bf16 v[68:71], v[226:229], v[32:35], v[68:71]
	v_mfma_f32_16x16x32_bf16 v[76:79], v[230:233], v[32:35], v[0:3]
	s_nop 2
	buffer_load_dwordx4 v[0:3], v160, s[20:23], s64 offen
	s_waitcnt lgkmcnt(2)
	v_mfma_f32_16x16x32_bf16 v[60:63], v[40:43], v[36:39], v[60:63]
	v_mfma_f32_16x16x32_bf16 v[56:59], v[222:225], v[36:39], v[56:59]
	v_mfma_f32_16x16x32_bf16 v[52:55], v[226:229], v[36:39], v[52:55]
	v_mfma_f32_16x16x32_bf16 v[48:51], v[230:233], v[36:39], v[48:51]
	s_waitcnt lgkmcnt(1)
	v_mfma_f32_16x16x32_bf16 v[40:43], v[40:43], v[144:147], v[44:47]
	s_waitcnt vmcnt(11)
	s_nop 1
	v_cvt_pk_bf16_f32 v45, v172, v173
	v_cvt_pk_bf16_f32 v44, v170, v171
	v_mfma_f32_16x16x32_bf16 v[36:39], v[222:225], v[144:147], v[174:177]
	ds_write_b64 v161, v[44:45] offset:26368
	v_mfma_f32_16x16x32_bf16 v[32:35], v[226:229], v[144:147], v[186:189]
	v_mfma_f32_16x16x32_bf16 v[44:47], v[230:233], v[144:147], v[16:19]
	s_nop 2
	buffer_load_dwordx4 v[16:19], v160, s[20:23], s66 offen
	s_waitcnt vmcnt(8)
	s_waitcnt lgkmcnt(0)
	s_barrier
	s_mov_b32 s100, 0x10000
	s_mov_b32 s101, 0
	v_mbcnt_lo_u32_b32 v144, -1, 0
	v_mbcnt_hi_u32_b32 v144, -1, v144
	s_and_b64 vcc, exec, s[14:15]
	v_and_or_b32 v145, v144, 15, s74
	v_ashrrev_i32_e32 v144, 1, v144
	v_and_b32_e32 v146, -8, v144
	v_add_u32_e32 v144, s51, v145
	s_ashr_i32 s51, s50, 31
	v_ashrrev_i32_e32 v147, 31, v146
	v_ashrrev_i32_e32 v145, 31, v144
	s_or_b64 s[8:9], s[50:51], s[28:29]
	v_lshlrev_b64 v[170:171], 11, v[144:145]
	v_lshl_add_u64 v[146:147], s[8:9], 0, v[146:147]
	v_lshl_add_u64 v[170:171], v[170:171], 0, v[146:147]
	v_lshlrev_b64 v[178:179], 1, v[170:171]
	v_lshl_add_u64 v[174:175], s[36:37], 0, v[178:179]
	v_mov_b32_e32 v198, v174
	v_mov_b32_e32 v199, v175
	global_load_dwordx4 v[170:173], v[174:175], off
	s_nop 0
	global_load_dwordx4 v[174:177], v[174:175], off offset:64
	v_lshl_add_u64 v[198:199], v[198:199], 0, s[100:101]
	global_load_dwordx4 v[208:211], v[198:199], off
	global_load_dwordx4 v[212:215], v[198:199], off offset:64
	v_add_u32_e32 v180, 16, v144
	v_ashrrev_i32_e32 v181, 31, v180
	v_lshlrev_b64 v[180:181], 11, v[180:181]
	v_lshl_add_u64 v[180:181], v[180:181], 0, v[146:147]
	v_lshl_add_u64 v[178:179], s[38:39], 0, v[178:179]
	v_lshlrev_b64 v[180:181], 1, v[180:181]
	v_lshl_add_u64 v[182:183], s[36:37], 0, v[180:181]
	s_mov_b64 s[20:21], s[18:19]
	s_mov_b64 s[22:23], s[10:11]
	s_mov_b64 s[18:19], s[10:11]
	s_mov_b64 s[14:15], s[10:11]
	s_mov_b32 s50, s52
	s_mov_b32 s51, s45
	s_waitcnt vmcnt(3)
	v_lshlrev_b32_e32 v184, 16, v170
	v_and_b32_e32 v185, 0xffff0000, v170
	v_lshlrev_b32_e32 v170, 16, v171
	v_and_b32_e32 v171, 0xffff0000, v171
	v_lshlrev_b32_e32 v186, 16, v172
	v_and_b32_e32 v187, 0xffff0000, v172
	v_lshlrev_b32_e32 v172, 16, v173
	v_and_b32_e32 v173, 0xffff0000, v173
	s_waitcnt vmcnt(2)
	v_lshlrev_b32_e32 v188, 16, v174
	v_and_b32_e32 v189, 0xffff0000, v174
	v_lshlrev_b32_e32 v174, 16, v175
	v_and_b32_e32 v175, 0xffff0000, v175
	v_lshlrev_b32_e32 v194, 16, v176
	v_and_b32_e32 v195, 0xffff0000, v176
	v_lshlrev_b32_e32 v176, 16, v177
	v_and_b32_e32 v177, 0xffff0000, v177
	v_pk_fma_f32 v[156:157], v[184:185], s[42:43], v[156:157] op_sel_hi:[1,0,1]
	v_pk_fma_f32 v[158:159], v[170:171], s[42:43], v[158:159] op_sel_hi:[1,0,1]
	v_pk_fma_f32 v[152:153], v[186:187], s[42:43], v[152:153] op_sel_hi:[1,0,1]
	v_pk_fma_f32 v[154:155], v[172:173], s[42:43], v[154:155] op_sel_hi:[1,0,1]
	v_pk_fma_f32 v[170:171], v[188:189], s[42:43], v[148:149] op_sel_hi:[1,0,1]
	v_pk_fma_f32 v[172:173], v[174:175], s[42:43], v[150:151] op_sel_hi:[1,0,1]
	v_pk_fma_f32 v[174:175], v[194:195], s[42:43], v[190:191] op_sel_hi:[1,0,1]
	v_pk_fma_f32 v[176:177], v[176:177], s[42:43], v[192:193] op_sel_hi:[1,0,1]
	v_cvt_pk_bf16_f32 v149, v158, v159
	v_cvt_pk_bf16_f32 v148, v156, v157
	v_cvt_pk_bf16_f32 v151, v154, v155
	v_cvt_pk_bf16_f32 v150, v152, v153
	v_cvt_pk_bf16_f32 v153, v172, v173
	v_cvt_pk_bf16_f32 v152, v170, v171
	v_cvt_pk_bf16_f32 v155, v176, v177
	v_cvt_pk_bf16_f32 v154, v174, v175
	global_store_dwordx4 v[178:179], v[148:151], off
	global_store_dwordx4 v[178:179], v[152:155], off offset:64
	v_lshl_add_u64 v[198:199], v[198:199], 0, s[100:101]
	global_load_dwordx4 v[200:203], v[198:199], off
	global_load_dwordx4 v[204:207], v[198:199], off offset:64
	s_nop 0
	v_add_u32_e32 v156, 32, v144
	v_ashrrev_i32_e32 v157, 31, v156
	v_lshlrev_b64 v[156:157], 11, v[156:157]
	v_lshl_add_u64 v[156:157], v[156:157], 0, v[146:147]
	v_lshlrev_b64 v[156:157], 1, v[156:157]
	v_lshl_add_u64 v[158:159], s[38:39], 0, v[180:181]
	v_lshl_add_u64 v[170:171], s[36:37], 0, v[156:157]
	s_waitcnt vmcnt(5)
	v_lshlrev_b32_e32 v172, 16, v208
	v_and_b32_e32 v173, 0xffff0000, v208
	v_lshlrev_b32_e32 v148, 16, v209
	v_and_b32_e32 v149, 0xffff0000, v209
	v_lshlrev_b32_e32 v174, 16, v210
	v_and_b32_e32 v175, 0xffff0000, v210
	v_lshlrev_b32_e32 v150, 16, v211
	v_and_b32_e32 v151, 0xffff0000, v211
	s_waitcnt vmcnt(4)
	v_lshlrev_b32_e32 v176, 16, v212
	v_and_b32_e32 v177, 0xffff0000, v212
	v_lshlrev_b32_e32 v152, 16, v213
	v_and_b32_e32 v153, 0xffff0000, v213
	v_lshlrev_b32_e32 v178, 16, v214
	v_and_b32_e32 v179, 0xffff0000, v214
	v_lshlrev_b32_e32 v154, 16, v215
	v_and_b32_e32 v155, 0xffff0000, v215
	v_pk_fma_f32 v[136:137], v[172:173], s[42:43], v[136:137] op_sel_hi:[1,0,1]
	v_pk_fma_f32 v[138:139], v[148:149], s[42:43], v[138:139] op_sel_hi:[1,0,1]
	v_pk_fma_f32 v[148:149], v[174:175], s[42:43], v[128:129] op_sel_hi:[1,0,1]
	v_pk_fma_f32 v[130:131], v[150:151], s[42:43], v[130:131] op_sel_hi:[1,0,1]
	v_pk_fma_f32 v[150:151], v[176:177], s[42:43], v[132:133] op_sel_hi:[1,0,1]
	v_pk_fma_f32 v[132:133], v[152:153], s[42:43], v[134:135] op_sel_hi:[1,0,1]
	v_pk_fma_f32 v[140:141], v[178:179], s[42:43], v[140:141] op_sel_hi:[1,0,1]
	v_pk_fma_f32 v[134:135], v[154:155], s[42:43], v[142:143] op_sel_hi:[1,0,1]
	v_cvt_pk_bf16_f32 v129, v138, v139
	v_cvt_pk_bf16_f32 v128, v136, v137
	v_cvt_pk_bf16_f32 v131, v130, v131
	v_cvt_pk_bf16_f32 v130, v148, v149
	v_cvt_pk_bf16_f32 v133, v132, v133
	v_cvt_pk_bf16_f32 v132, v150, v151
	v_cvt_pk_bf16_f32 v135, v134, v135
	v_cvt_pk_bf16_f32 v134, v140, v141
	global_store_dwordx4 v[158:159], v[128:131], off
	global_store_dwordx4 v[158:159], v[132:135], off offset:64
	v_lshl_add_u64 v[198:199], v[198:199], 0, s[100:101]
	global_load_dwordx4 v[208:211], v[198:199], off
	global_load_dwordx4 v[212:215], v[198:199], off offset:64
	s_nop 0
	v_add_u32_e32 v136, 48, v144
	v_ashrrev_i32_e32 v137, 31, v136
	v_lshlrev_b64 v[136:137], 11, v[136:137]
	v_lshl_add_u64 v[136:137], v[136:137], 0, v[146:147]
	v_lshlrev_b64 v[136:137], 1, v[136:137]
	v_lshl_add_u64 v[138:139], s[38:39], 0, v[156:157]
	v_lshl_add_u64 v[140:141], s[36:37], 0, v[136:137]
	s_waitcnt vmcnt(5)
	v_lshlrev_b32_e32 v142, 16, v200
	v_and_b32_e32 v143, 0xffff0000, v200
	v_lshlrev_b32_e32 v128, 16, v201
	v_and_b32_e32 v129, 0xffff0000, v201
	v_lshlrev_b32_e32 v148, 16, v202
	v_and_b32_e32 v149, 0xffff0000, v202
	v_lshlrev_b32_e32 v130, 16, v203
	v_and_b32_e32 v131, 0xffff0000, v203
	s_waitcnt vmcnt(4)
	v_lshlrev_b32_e32 v150, 16, v204
	v_and_b32_e32 v151, 0xffff0000, v204
	v_lshlrev_b32_e32 v132, 16, v205
	v_and_b32_e32 v133, 0xffff0000, v205
	v_lshlrev_b32_e32 v152, 16, v206
	v_and_b32_e32 v153, 0xffff0000, v206
	v_lshlrev_b32_e32 v134, 16, v207
	v_and_b32_e32 v135, 0xffff0000, v207
	v_pk_fma_f32 v[124:125], v[142:143], s[42:43], v[124:125] op_sel_hi:[1,0,1]
	v_pk_fma_f32 v[126:127], v[128:129], s[42:43], v[126:127] op_sel_hi:[1,0,1]
	v_pk_fma_f32 v[120:121], v[148:149], s[42:43], v[120:121] op_sel_hi:[1,0,1]
	v_pk_fma_f32 v[122:123], v[130:131], s[42:43], v[122:123] op_sel_hi:[1,0,1]
	v_pk_fma_f32 v[128:129], v[150:151], s[42:43], v[112:113] op_sel_hi:[1,0,1]
	v_pk_fma_f32 v[130:131], v[132:133], s[42:43], v[114:115] op_sel_hi:[1,0,1]
	v_pk_fma_f32 v[132:133], v[152:153], s[42:43], v[116:117] op_sel_hi:[1,0,1]
	v_pk_fma_f32 v[118:119], v[134:135], s[42:43], v[118:119] op_sel_hi:[1,0,1]
	v_cvt_pk_bf16_f32 v113, v126, v127
	v_cvt_pk_bf16_f32 v112, v124, v125
	v_cvt_pk_bf16_f32 v115, v122, v123
	v_cvt_pk_bf16_f32 v114, v120, v121
	v_cvt_pk_bf16_f32 v117, v130, v131
	v_cvt_pk_bf16_f32 v116, v128, v129
	v_cvt_pk_bf16_f32 v119, v118, v119
	v_cvt_pk_bf16_f32 v118, v132, v133
	global_store_dwordx4 v[138:139], v[112:115], off
	global_store_dwordx4 v[138:139], v[116:119], off offset:64
	v_lshl_add_u64 v[198:199], v[198:199], 0, s[100:101]
	global_load_dwordx4 v[200:203], v[198:199], off
	global_load_dwordx4 v[204:207], v[198:199], off offset:64
	s_nop 0
	v_add_u32_e32 v120, 64, v144
	v_ashrrev_i32_e32 v121, 31, v120
	v_lshlrev_b64 v[120:121], 11, v[120:121]
	v_lshl_add_u64 v[120:121], v[120:121], 0, v[146:147]
	v_lshlrev_b64 v[120:121], 1, v[120:121]
	v_lshl_add_u64 v[122:123], s[38:39], 0, v[136:137]
	v_lshl_add_u64 v[124:125], s[36:37], 0, v[120:121]
	s_waitcnt vmcnt(5)
	v_lshlrev_b32_e32 v126, 16, v208
	v_and_b32_e32 v127, 0xffff0000, v208
	v_lshlrev_b32_e32 v112, 16, v209
	v_and_b32_e32 v113, 0xffff0000, v209
	v_lshlrev_b32_e32 v128, 16, v210
	v_and_b32_e32 v129, 0xffff0000, v210
	v_lshlrev_b32_e32 v114, 16, v211
	v_and_b32_e32 v115, 0xffff0000, v211
	s_waitcnt vmcnt(4)
	v_lshlrev_b32_e32 v130, 16, v212
	v_and_b32_e32 v131, 0xffff0000, v212
	v_lshlrev_b32_e32 v116, 16, v213
	v_and_b32_e32 v117, 0xffff0000, v213
	v_lshlrev_b32_e32 v132, 16, v214
	v_and_b32_e32 v133, 0xffff0000, v214
	v_lshlrev_b32_e32 v118, 16, v215
	v_and_b32_e32 v119, 0xffff0000, v215
	v_pk_fma_f32 v[104:105], v[126:127], s[42:43], v[104:105] op_sel_hi:[1,0,1]
	v_pk_fma_f32 v[106:107], v[112:113], s[42:43], v[106:107] op_sel_hi:[1,0,1]
	v_pk_fma_f32 v[112:113], v[128:129], s[42:43], v[96:97] op_sel_hi:[1,0,1]
	v_pk_fma_f32 v[98:99], v[114:115], s[42:43], v[98:99] op_sel_hi:[1,0,1]
	v_pk_fma_f32 v[114:115], v[130:131], s[42:43], v[100:101] op_sel_hi:[1,0,1]
	v_pk_fma_f32 v[100:101], v[116:117], s[42:43], v[102:103] op_sel_hi:[1,0,1]
	v_pk_fma_f32 v[108:109], v[132:133], s[42:43], v[108:109] op_sel_hi:[1,0,1]
	v_pk_fma_f32 v[102:103], v[118:119], s[42:43], v[110:111] op_sel_hi:[1,0,1]
	v_cvt_pk_bf16_f32 v97, v106, v107
	v_cvt_pk_bf16_f32 v96, v104, v105
	v_cvt_pk_bf16_f32 v99, v98, v99
	v_cvt_pk_bf16_f32 v98, v112, v113
	v_cvt_pk_bf16_f32 v101, v100, v101
	v_cvt_pk_bf16_f32 v100, v114, v115
	v_cvt_pk_bf16_f32 v103, v102, v103
	v_cvt_pk_bf16_f32 v102, v108, v109
	global_store_dwordx4 v[122:123], v[96:99], off
	global_store_dwordx4 v[122:123], v[100:103], off offset:64
	v_lshl_add_u64 v[198:199], v[198:199], 0, s[100:101]
	global_load_dwordx4 v[208:211], v[198:199], off
	global_load_dwordx4 v[212:215], v[198:199], off offset:64
	s_nop 0
	v_add_u32_e32 v104, 0x50, v144
	v_ashrrev_i32_e32 v105, 31, v104
	v_lshlrev_b64 v[104:105], 11, v[104:105]
	v_lshl_add_u64 v[104:105], v[104:105], 0, v[146:147]
	v_lshlrev_b64 v[104:105], 1, v[104:105]
	v_lshl_add_u64 v[106:107], s[38:39], 0, v[120:121]
	v_lshl_add_u64 v[108:109], s[36:37], 0, v[104:105]
	s_waitcnt vmcnt(5)
	v_lshlrev_b32_e32 v110, 16, v200
	v_and_b32_e32 v111, 0xffff0000, v200
	v_lshlrev_b32_e32 v96, 16, v201
	v_and_b32_e32 v97, 0xffff0000, v201
	v_lshlrev_b32_e32 v112, 16, v202
	v_and_b32_e32 v113, 0xffff0000, v202
	v_lshlrev_b32_e32 v98, 16, v203
	v_and_b32_e32 v99, 0xffff0000, v203
	s_waitcnt vmcnt(4)
	v_lshlrev_b32_e32 v114, 16, v204
	v_and_b32_e32 v115, 0xffff0000, v204
	v_lshlrev_b32_e32 v100, 16, v205
	v_and_b32_e32 v101, 0xffff0000, v205
	v_lshlrev_b32_e32 v116, 16, v206
	v_and_b32_e32 v117, 0xffff0000, v206
	v_lshlrev_b32_e32 v102, 16, v207
	v_and_b32_e32 v103, 0xffff0000, v207
	v_pk_fma_f32 v[92:93], v[110:111], s[42:43], v[92:93] op_sel_hi:[1,0,1]
	v_pk_fma_f32 v[94:95], v[96:97], s[42:43], v[94:95] op_sel_hi:[1,0,1]
	v_pk_fma_f32 v[88:89], v[112:113], s[42:43], v[88:89] op_sel_hi:[1,0,1]
	v_pk_fma_f32 v[90:91], v[98:99], s[42:43], v[90:91] op_sel_hi:[1,0,1]
	v_pk_fma_f32 v[96:97], v[114:115], s[42:43], v[80:81] op_sel_hi:[1,0,1]
	v_pk_fma_f32 v[98:99], v[100:101], s[42:43], v[82:83] op_sel_hi:[1,0,1]
	v_pk_fma_f32 v[100:101], v[116:117], s[42:43], v[84:85] op_sel_hi:[1,0,1]
	v_pk_fma_f32 v[86:87], v[102:103], s[42:43], v[86:87] op_sel_hi:[1,0,1]
	v_cvt_pk_bf16_f32 v81, v94, v95
	v_cvt_pk_bf16_f32 v80, v92, v93
	v_cvt_pk_bf16_f32 v83, v90, v91
	v_cvt_pk_bf16_f32 v82, v88, v89
	v_cvt_pk_bf16_f32 v85, v98, v99
	v_cvt_pk_bf16_f32 v84, v96, v97
	v_cvt_pk_bf16_f32 v87, v86, v87
	v_cvt_pk_bf16_f32 v86, v100, v101
	global_store_dwordx4 v[106:107], v[80:83], off
	global_store_dwordx4 v[106:107], v[84:87], off offset:64
	v_lshl_add_u64 v[198:199], v[198:199], 0, s[100:101]
	global_load_dwordx4 v[200:203], v[198:199], off
	global_load_dwordx4 v[204:207], v[198:199], off offset:64
	s_nop 0
	v_add_u32_e32 v88, 0x60, v144
	v_ashrrev_i32_e32 v89, 31, v88
	v_lshlrev_b64 v[88:89], 11, v[88:89]
	v_lshl_add_u64 v[88:89], v[88:89], 0, v[146:147]
	v_lshlrev_b64 v[88:89], 1, v[88:89]
	v_lshl_add_u64 v[90:91], s[38:39], 0, v[104:105]
	v_lshl_add_u64 v[92:93], s[36:37], 0, v[88:89]
	s_waitcnt vmcnt(5)
	v_lshlrev_b32_e32 v94, 16, v208
	v_and_b32_e32 v95, 0xffff0000, v208
	v_lshlrev_b32_e32 v80, 16, v209
	v_and_b32_e32 v81, 0xffff0000, v209
	v_lshlrev_b32_e32 v96, 16, v210
	v_and_b32_e32 v97, 0xffff0000, v210
	v_lshlrev_b32_e32 v82, 16, v211
	v_and_b32_e32 v83, 0xffff0000, v211
	s_waitcnt vmcnt(4)
	v_lshlrev_b32_e32 v98, 16, v212
	v_and_b32_e32 v99, 0xffff0000, v212
	v_lshlrev_b32_e32 v84, 16, v213
	v_and_b32_e32 v85, 0xffff0000, v213
	v_lshlrev_b32_e32 v100, 16, v214
	v_and_b32_e32 v101, 0xffff0000, v214
	v_lshlrev_b32_e32 v86, 16, v215
	v_and_b32_e32 v87, 0xffff0000, v215
	v_pk_fma_f32 v[72:73], v[94:95], s[42:43], v[72:73] op_sel_hi:[1,0,1]
	v_pk_fma_f32 v[74:75], v[80:81], s[42:43], v[74:75] op_sel_hi:[1,0,1]
	v_pk_fma_f32 v[80:81], v[96:97], s[42:43], v[64:65] op_sel_hi:[1,0,1]
	v_pk_fma_f32 v[66:67], v[82:83], s[42:43], v[66:67] op_sel_hi:[1,0,1]
	v_pk_fma_f32 v[82:83], v[98:99], s[42:43], v[68:69] op_sel_hi:[1,0,1]
	v_pk_fma_f32 v[68:69], v[84:85], s[42:43], v[70:71] op_sel_hi:[1,0,1]
	v_pk_fma_f32 v[76:77], v[100:101], s[42:43], v[76:77] op_sel_hi:[1,0,1]
	v_pk_fma_f32 v[70:71], v[86:87], s[42:43], v[78:79] op_sel_hi:[1,0,1]
	v_cvt_pk_bf16_f32 v65, v74, v75
	v_cvt_pk_bf16_f32 v64, v72, v73
	v_cvt_pk_bf16_f32 v67, v66, v67
	v_cvt_pk_bf16_f32 v66, v80, v81
	v_cvt_pk_bf16_f32 v69, v68, v69
	v_cvt_pk_bf16_f32 v68, v82, v83
	v_cvt_pk_bf16_f32 v71, v70, v71
	v_cvt_pk_bf16_f32 v70, v76, v77
	global_store_dwordx4 v[90:91], v[64:67], off
	global_store_dwordx4 v[90:91], v[68:71], off offset:64
	v_lshl_add_u64 v[198:199], v[198:199], 0, s[100:101]
	global_load_dwordx4 v[208:211], v[198:199], off
	global_load_dwordx4 v[212:215], v[198:199], off offset:64
	s_nop 0
	v_add_u32_e32 v72, 0x70, v144
	v_ashrrev_i32_e32 v73, 31, v72
	v_lshlrev_b64 v[72:73], 11, v[72:73]
	v_lshl_add_u64 v[72:73], v[72:73], 0, v[146:147]
	v_lshlrev_b64 v[72:73], 1, v[72:73]
	v_lshl_add_u64 v[74:75], s[38:39], 0, v[88:89]
	v_lshl_add_u64 v[76:77], s[36:37], 0, v[72:73]
	s_waitcnt vmcnt(5)
	v_lshlrev_b32_e32 v78, 16, v200
	v_and_b32_e32 v79, 0xffff0000, v200
	v_lshlrev_b32_e32 v64, 16, v201
	v_and_b32_e32 v65, 0xffff0000, v201
	v_lshlrev_b32_e32 v80, 16, v202
	v_and_b32_e32 v81, 0xffff0000, v202
	v_lshlrev_b32_e32 v66, 16, v203
	v_and_b32_e32 v67, 0xffff0000, v203
	s_waitcnt vmcnt(4)
	v_lshlrev_b32_e32 v82, 16, v204
	v_and_b32_e32 v83, 0xffff0000, v204
	v_lshlrev_b32_e32 v68, 16, v205
	v_and_b32_e32 v69, 0xffff0000, v205
	v_lshlrev_b32_e32 v84, 16, v206
	v_and_b32_e32 v85, 0xffff0000, v206
	v_lshlrev_b32_e32 v70, 16, v207
	v_and_b32_e32 v71, 0xffff0000, v207
	v_pk_fma_f32 v[60:61], v[78:79], s[42:43], v[60:61] op_sel_hi:[1,0,1]
	v_pk_fma_f32 v[62:63], v[64:65], s[42:43], v[62:63] op_sel_hi:[1,0,1]
	v_pk_fma_f32 v[56:57], v[80:81], s[42:43], v[56:57] op_sel_hi:[1,0,1]
	v_pk_fma_f32 v[58:59], v[66:67], s[42:43], v[58:59] op_sel_hi:[1,0,1]
	v_pk_fma_f32 v[64:65], v[82:83], s[42:43], v[52:53] op_sel_hi:[1,0,1]
	v_pk_fma_f32 v[52:53], v[68:69], s[42:43], v[54:55] op_sel_hi:[1,0,1]
	v_pk_fma_f32 v[66:67], v[84:85], s[42:43], v[48:49] op_sel_hi:[1,0,1]
	v_pk_fma_f32 v[54:55], v[70:71], s[42:43], v[50:51] op_sel_hi:[1,0,1]
	v_cvt_pk_bf16_f32 v49, v62, v63
	v_cvt_pk_bf16_f32 v48, v60, v61
	v_cvt_pk_bf16_f32 v51, v58, v59
	v_cvt_pk_bf16_f32 v50, v56, v57
	v_cvt_pk_bf16_f32 v53, v52, v53
	v_cvt_pk_bf16_f32 v52, v64, v65
	v_cvt_pk_bf16_f32 v55, v54, v55
	v_cvt_pk_bf16_f32 v54, v66, v67
	global_store_dwordx4 v[74:75], v[48:51], off
	global_store_dwordx4 v[74:75], v[52:55], off offset:64
	s_nop 0
	v_lshl_add_u64 v[56:57], s[38:39], 0, v[72:73]
	s_waitcnt vmcnt(3)
	v_lshlrev_b32_e32 v58, 16, v208
	v_and_b32_e32 v59, 0xffff0000, v208
	v_lshlrev_b32_e32 v48, 16, v209
	v_and_b32_e32 v49, 0xffff0000, v209
	v_lshlrev_b32_e32 v60, 16, v210
	v_and_b32_e32 v61, 0xffff0000, v210
	v_lshlrev_b32_e32 v50, 16, v211
	v_and_b32_e32 v51, 0xffff0000, v211
	s_waitcnt vmcnt(2)
	v_lshlrev_b32_e32 v62, 16, v212
	v_and_b32_e32 v63, 0xffff0000, v212
	v_lshlrev_b32_e32 v52, 16, v213
	v_and_b32_e32 v53, 0xffff0000, v213
	v_lshlrev_b32_e32 v64, 16, v214
	v_and_b32_e32 v65, 0xffff0000, v214
	v_lshlrev_b32_e32 v54, 16, v215
	v_and_b32_e32 v55, 0xffff0000, v215
	v_pk_fma_f32 v[40:41], v[58:59], s[42:43], v[40:41] op_sel_hi:[1,0,1]
	v_pk_fma_f32 v[42:43], v[48:49], s[42:43], v[42:43] op_sel_hi:[1,0,1]
	v_pk_fma_f32 v[36:37], v[60:61], s[42:43], v[36:37] op_sel_hi:[1,0,1]
	v_pk_fma_f32 v[38:39], v[50:51], s[42:43], v[38:39] op_sel_hi:[1,0,1]
	v_pk_fma_f32 v[48:49], v[62:63], s[42:43], v[32:33] op_sel_hi:[1,0,1]
	v_pk_fma_f32 v[50:51], v[52:53], s[42:43], v[34:35] op_sel_hi:[1,0,1]
	v_pk_fma_f32 v[44:45], v[64:65], s[42:43], v[44:45] op_sel_hi:[1,0,1]
	v_pk_fma_f32 v[46:47], v[54:55], s[42:43], v[46:47] op_sel_hi:[1,0,1]
	v_cvt_pk_bf16_f32 v33, v42, v43
	v_cvt_pk_bf16_f32 v32, v40, v41
	v_cvt_pk_bf16_f32 v35, v38, v39
	v_cvt_pk_bf16_f32 v34, v36, v37
	v_cvt_pk_bf16_f32 v37, v50, v51
	v_cvt_pk_bf16_f32 v36, v48, v49
	v_cvt_pk_bf16_f32 v39, v46, v47
	v_cvt_pk_bf16_f32 v38, v44, v45
	global_store_dwordx4 v[56:57], v[32:35], off
	global_store_dwordx4 v[56:57], v[36:39], off offset:64
	s_cbranch_vccnz .LBB0_382

.LBB0_1035:
	s_mov_b32 m0, s64
	ds_read_b64_tr_b16 v[160:161], v178
	ds_read_b64_tr_b16 v[164:165], v178 offset:32
	ds_read_b64_tr_b16 v[168:169], v178 offset:64
	ds_read_b64_tr_b16 v[182:183], v178 offset:96
	ds_read_b64_tr_b16 v[162:163], v179
	ds_read_b64_tr_b16 v[166:167], v179 offset:32
	ds_read_b64_tr_b16 v[170:171], v179 offset:64
	ds_read_b64_tr_b16 v[184:185], v179 offset:96
	ds_read_b128 v[186:189], v175
	ds_read_b128 v[190:193], v175 offset:2048
	ds_read_b128 v[194:197], v175 offset:4096
	buffer_load_dwordx4 v176, s[16:19], s65 offen lds
	s_mov_b32 m0, s63
	s_and_b32 s13, s48, 0xffff
	buffer_load_dwordx4 v177, s[16:19], s65 offen lds
	s_mov_b32 m0, s62
	s_and_b32 s9, s46, 0xffff
	buffer_load_dwordx4 v180, s[16:19], s65 offen lds
	s_mov_b32 m0, s61
	s_mov_b32 s8, s37
	buffer_load_dwordx4 v181, s[16:19], s65 offen lds
	v_mbcnt_lo_u32_b32 v172, -1, 0
	v_mbcnt_hi_u32_b32 v172, -1, v172
	s_mov_b32 s12, s47
	v_lshlrev_b32_e32 v176, 4, v172
	v_and_b32_e32 v177, 32, v172
	v_lshrrev_b32_e32 v172, 2, v172
	v_bitop3_b32 v176, v176, v177, 48 bitop3:0x6c
	v_add_lshl_u32 v172, v172, s49, 12
	v_or3_b32 v176, v176, s50, v172
	s_mov_b32 s16, s47
	s_mov_b32 s17, s13
	s_mov_b32 s18, s2
	s_mov_b32 s19, s3
	s_and_b32 s11, s44, 0xffff
	s_mov_b32 s10, s43
	v_add_u32_e32 v177, 0x40000, v176
	v_add_u32_e32 v180, 0x80000, v176
	v_add_u32_e32 v181, 0xc0000, v176
	s_mov_b32 s0, s37
	s_mov_b32 s1, s9
	s_mov_b32 s20, s43
	s_mov_b32 s21, s11
	s_mov_b32 s22, s2
	s_mov_b32 s23, s3
	s_waitcnt lgkmcnt(2)
	v_mfma_f32_16x16x32_bf16 v[156:159], v[160:163], v[186:189], v[156:159]
	v_mfma_f32_16x16x32_bf16 v[152:155], v[164:167], v[186:189], v[152:155]
	v_mfma_f32_16x16x32_bf16 v[148:151], v[168:171], v[186:189], v[148:151]
	v_mfma_f32_16x16x32_bf16 v[144:147], v[182:185], v[186:189], v[144:147]
	s_waitcnt vmcnt(11)
	v_cvt_pk_bf16_f32 v15, v14, v15
	v_cvt_pk_bf16_f32 v14, v12, v13
	ds_read_b128 v[186:189], v175 offset:6144
	ds_write_b64 v174, v[14:15] offset:34816
	s_waitcnt lgkmcnt(3)
	v_mfma_f32_16x16x32_bf16 v[12:15], v[182:185], v[190:193], v[128:131]
	v_mfma_f32_16x16x32_bf16 v[140:143], v[160:163], v[190:193], v[140:143]
	v_mfma_f32_16x16x32_bf16 v[136:139], v[164:167], v[190:193], v[136:139]
	v_mfma_f32_16x16x32_bf16 v[132:135], v[168:171], v[190:193], v[132:135]
	buffer_load_dwordx4 v[128:131], v173, s[0:3], 0 offen
	ds_read_b128 v[190:193], v175 offset:8192
	s_waitcnt lgkmcnt(3)
	v_mfma_f32_16x16x32_bf16 v[124:127], v[160:163], v[194:197], v[124:127]
	v_mfma_f32_16x16x32_bf16 v[120:123], v[164:167], v[194:197], v[120:123]
	v_mfma_f32_16x16x32_bf16 v[116:119], v[168:171], v[194:197], v[116:119]
	v_mfma_f32_16x16x32_bf16 v[112:115], v[182:185], v[194:197], v[112:115]
	s_waitcnt vmcnt(10)
	v_cvt_pk_bf16_f32 v31, v30, v31
	v_cvt_pk_bf16_f32 v30, v28, v29
	ds_read_b128 v[194:197], v175 offset:10240
	ds_write_b64 v174, v[30:31] offset:43520
	s_waitcnt lgkmcnt(4)
	v_mfma_f32_16x16x32_bf16 v[28:31], v[182:185], v[186:189], v[96:99]
	v_mfma_f32_16x16x32_bf16 v[108:111], v[160:163], v[186:189], v[108:111]
	v_mfma_f32_16x16x32_bf16 v[104:107], v[164:167], v[186:189], v[104:107]
	v_mfma_f32_16x16x32_bf16 v[100:103], v[168:171], v[186:189], v[100:103]
	buffer_load_dwordx4 v[96:99], v173, s[0:3], s3 offen
	ds_read_b128 v[186:189], v175 offset:12288
	s_waitcnt lgkmcnt(3)
	v_mfma_f32_16x16x32_bf16 v[92:95], v[160:163], v[190:193], v[92:95]
	v_mfma_f32_16x16x32_bf16 v[88:91], v[164:167], v[190:193], v[88:91]
	v_mfma_f32_16x16x32_bf16 v[84:87], v[168:171], v[190:193], v[84:87]
	v_mfma_f32_16x16x32_bf16 v[80:83], v[182:185], v[190:193], v[80:83]
	v_cvt_pk_bf16_f32 v7, v6, v7
	v_cvt_pk_bf16_f32 v6, v4, v5
	ds_read_b128 v[190:193], v175 offset:14336
	ds_write_b64 v174, v[6:7] offset:52224
	s_waitcnt lgkmcnt(4)
	v_mfma_f32_16x16x32_bf16 v[4:7], v[182:185], v[194:197], v[64:67]
	v_mfma_f32_16x16x32_bf16 v[76:79], v[160:163], v[194:197], v[76:79]
	v_mfma_f32_16x16x32_bf16 v[72:75], v[164:167], v[194:197], v[72:75]
	v_mfma_f32_16x16x32_bf16 v[68:71], v[168:171], v[194:197], v[68:71]
	buffer_load_dwordx4 v[64:67], v173, s[0:3], s51 offen
	ds_read_b128 v[194:197], v175 offset:1024
	s_waitcnt lgkmcnt(3)
	v_mfma_f32_16x16x32_bf16 v[60:63], v[160:163], v[186:189], v[60:63]
	v_mfma_f32_16x16x32_bf16 v[56:59], v[164:167], v[186:189], v[56:59]
	v_mfma_f32_16x16x32_bf16 v[52:55], v[168:171], v[186:189], v[52:55]
	v_mfma_f32_16x16x32_bf16 v[48:51], v[182:185], v[186:189], v[48:51]
	s_waitcnt lgkmcnt(2)
	v_mfma_f32_16x16x32_bf16 v[44:47], v[160:163], v[190:193], v[44:47]
	ds_read_b128 v[160:163], v175 offset:3072
	v_mfma_f32_16x16x32_bf16 v[40:43], v[164:167], v[190:193], v[40:43]
	ds_read_b64_tr_b16 v[164:165], v178 offset:17408
	ds_read_b64_tr_b16 v[186:187], v178 offset:17440
	ds_read_b64_tr_b16 v[198:199], v178 offset:17472
	ds_read_b64_tr_b16 v[202:203], v178 offset:17504
	ds_read_b64_tr_b16 v[166:167], v179 offset:17408
	ds_read_b64_tr_b16 v[188:189], v179 offset:17440
	ds_read_b64_tr_b16 v[200:201], v179 offset:17472
	ds_read_b64_tr_b16 v[204:205], v179 offset:17504
	v_mfma_f32_16x16x32_bf16 v[36:39], v[168:171], v[190:193], v[36:39]
	s_waitcnt vmcnt(11)
	v_cvt_pk_bf16_f32 v169, v26, v27
	v_cvt_pk_bf16_f32 v168, v24, v25
	ds_write_b64 v174, v[168:169] offset:60928
	v_mfma_f32_16x16x32_bf16 v[24:27], v[182:185], v[190:193], v[32:35]
	s_nop 2
	buffer_load_dwordx4 v[32:35], v173, s[0:3], s52 offen
	ds_read_b128 v[168:171], v175 offset:5120
	s_waitcnt lgkmcnt(5)
	v_mfma_f32_16x16x32_bf16 v[156:159], v[164:167], v[194:197], v[156:159]
	s_waitcnt lgkmcnt(4)
	v_mfma_f32_16x16x32_bf16 v[152:155], v[186:189], v[194:197], v[152:155]
	s_waitcnt lgkmcnt(3)
	v_mfma_f32_16x16x32_bf16 v[148:151], v[198:201], v[194:197], v[148:151]
	s_waitcnt lgkmcnt(2)
	v_mfma_f32_16x16x32_bf16 v[144:147], v[202:205], v[194:197], v[144:147]
	ds_read_b128 v[182:185], v175 offset:7168
	v_mfma_f32_16x16x32_bf16 v[12:15], v[202:205], v[160:163], v[12:15]
	s_waitcnt vmcnt(11)
	v_cvt_pk_bf16_f32 v23, v22, v23
	v_cvt_pk_bf16_f32 v22, v20, v21
	ds_write_b64 v174, v[22:23] offset:35072
	v_mfma_f32_16x16x32_bf16 v[140:143], v[164:167], v[160:163], v[140:143]
	v_mfma_f32_16x16x32_bf16 v[136:139], v[186:189], v[160:163], v[136:139]
	v_mfma_f32_16x16x32_bf16 v[132:135], v[198:201], v[160:163], v[132:135]
	buffer_load_dwordx4 v[20:23], v173, s[16:19], 0 offen
	ds_read_b128 v[160:163], v175 offset:9216
	s_waitcnt lgkmcnt(3)
	v_mfma_f32_16x16x32_bf16 v[124:127], v[164:167], v[168:171], v[124:127]
	v_mfma_f32_16x16x32_bf16 v[120:123], v[186:189], v[168:171], v[120:123]
	v_mfma_f32_16x16x32_bf16 v[116:119], v[198:201], v[168:171], v[116:119]
	v_mfma_f32_16x16x32_bf16 v[112:115], v[202:205], v[168:171], v[112:115]
	s_waitcnt vmcnt(10)
	v_cvt_pk_bf16_f32 v11, v10, v11
	v_cvt_pk_bf16_f32 v10, v8, v9
	ds_read_b128 v[168:171], v175 offset:11264
	ds_write_b64 v174, v[10:11] offset:43776
	s_waitcnt lgkmcnt(4)
	v_mfma_f32_16x16x32_bf16 v[8:11], v[202:205], v[182:185], v[28:31]
	v_mfma_f32_16x16x32_bf16 v[108:111], v[164:167], v[182:185], v[108:111]
	v_mfma_f32_16x16x32_bf16 v[104:107], v[186:189], v[182:185], v[104:107]
	v_mfma_f32_16x16x32_bf16 v[100:103], v[198:201], v[182:185], v[100:103]
	buffer_load_dwordx4 v[182:185], v173, s[16:19], s3 offen
	ds_read_b128 v[28:31], v175 offset:13312
	s_waitcnt lgkmcnt(3)
	v_mfma_f32_16x16x32_bf16 v[92:95], v[164:167], v[160:163], v[92:95]
	v_mfma_f32_16x16x32_bf16 v[88:91], v[186:189], v[160:163], v[88:91]
	v_mfma_f32_16x16x32_bf16 v[84:87], v[198:201], v[160:163], v[84:87]
	v_mfma_f32_16x16x32_bf16 v[80:83], v[202:205], v[160:163], v[80:83]
	v_cvt_pk_bf16_f32 v3, v2, v3
	v_cvt_pk_bf16_f32 v2, v0, v1
	ds_read_b128 v[160:163], v175 offset:15360
	ds_write_b64 v174, v[2:3] offset:52480
	s_waitcnt lgkmcnt(4)
	v_mfma_f32_16x16x32_bf16 v[0:3], v[202:205], v[168:171], v[4:7]
	v_mfma_f32_16x16x32_bf16 v[76:79], v[164:167], v[168:171], v[76:79]
	v_mfma_f32_16x16x32_bf16 v[72:75], v[186:189], v[168:171], v[72:75]
	v_mfma_f32_16x16x32_bf16 v[68:71], v[198:201], v[168:171], v[68:71]
	buffer_load_dwordx4 v[168:171], v173, s[16:19], s51 offen
	s_waitcnt lgkmcnt(2)
	v_mfma_f32_16x16x32_bf16 v[60:63], v[164:167], v[28:31], v[60:63]
	v_mfma_f32_16x16x32_bf16 v[56:59], v[186:189], v[28:31], v[56:59]
	v_mfma_f32_16x16x32_bf16 v[52:55], v[198:201], v[28:31], v[52:55]
	v_mfma_f32_16x16x32_bf16 v[48:51], v[202:205], v[28:31], v[48:51]
	s_waitcnt vmcnt(11)
	v_cvt_pk_bf16_f32 v5, v18, v19
	v_cvt_pk_bf16_f32 v4, v16, v17
	s_waitcnt lgkmcnt(1)
	v_mfma_f32_16x16x32_bf16 v[16:19], v[202:205], v[160:163], v[24:27]
	ds_write_b64 v174, v[4:5] offset:61184
	v_mfma_f32_16x16x32_bf16 v[44:47], v[164:167], v[160:163], v[44:47]
	v_mfma_f32_16x16x32_bf16 v[40:43], v[186:189], v[160:163], v[40:43]
	v_mfma_f32_16x16x32_bf16 v[36:39], v[198:201], v[160:163], v[36:39]
	buffer_load_dwordx4 v[186:189], v173, s[16:19], s52 offen
	s_waitcnt vmcnt(8)
	s_mov_b32 m0, s45
	s_waitcnt lgkmcnt(0)
	s_barrier
	ds_read_b64_tr_b16 v[24:25], v178 offset:34816
	ds_read_b64_tr_b16 v[26:27], v179 offset:34816
	ds_read_b64_tr_b16 v[162:163], v179 offset:34848
	ds_read_b128 v[4:7], v175 offset:32768
	ds_read_b64_tr_b16 v[160:161], v178 offset:34848
	ds_read_b64_tr_b16 v[164:165], v178 offset:34880
	ds_read_b64_tr_b16 v[190:191], v178 offset:34912
	ds_read_b64_tr_b16 v[166:167], v179 offset:34880
	ds_read_b64_tr_b16 v[192:193], v179 offset:34912
	ds_read_b128 v[28:31], v175 offset:34816
	ds_read_b128 v[194:197], v175 offset:36864
	buffer_load_dwordx4 v176, s[20:23], 0 offen lds
	s_mov_b32 m0, s53
	s_waitcnt lgkmcnt(7)
	v_mfma_f32_16x16x32_bf16 v[156:159], v[24:27], v[4:7], v[156:159]
	buffer_load_dwordx4 v177, s[20:23], 0 offen lds
	s_mov_b32 m0, s54
	s_nop 0
	buffer_load_dwordx4 v180, s[20:23], 0 offen lds
	s_mov_b32 m0, s55
	s_waitcnt lgkmcnt(6)
	v_mfma_f32_16x16x32_bf16 v[152:155], v[160:163], v[4:7], v[152:155]
	buffer_load_dwordx4 v181, s[20:23], 0 offen lds
	s_waitcnt lgkmcnt(3)
	v_mfma_f32_16x16x32_bf16 v[148:151], v[164:167], v[4:7], v[148:151]
	s_waitcnt lgkmcnt(2)
	v_mfma_f32_16x16x32_bf16 v[144:147], v[190:193], v[4:7], v[144:147]
	ds_read_b128 v[4:7], v175 offset:38912
	s_waitcnt vmcnt(11)
	v_cvt_pk_bf16_f32 v131, v130, v131
	v_cvt_pk_bf16_f32 v130, v128, v129
	s_waitcnt lgkmcnt(2)
	v_mfma_f32_16x16x32_bf16 v[140:143], v[24:27], v[28:31], v[140:143]
	ds_write_b64 v174, v[130:131]
	v_mfma_f32_16x16x32_bf16 v[136:139], v[160:163], v[28:31], v[136:139]
	v_mfma_f32_16x16x32_bf16 v[132:135], v[164:167], v[28:31], v[132:135]
	v_mfma_f32_16x16x32_bf16 v[128:131], v[190:193], v[28:31], v[12:15]
	s_nop 2
	buffer_load_dwordx4 v[12:15], v173, s[0:3], s56 offen
	ds_read_b128 v[198:201], v175 offset:40960
	s_waitcnt lgkmcnt(3)
	v_mfma_f32_16x16x32_bf16 v[124:127], v[24:27], v[194:197], v[124:127]
	v_mfma_f32_16x16x32_bf16 v[120:123], v[160:163], v[194:197], v[120:123]
	v_mfma_f32_16x16x32_bf16 v[116:119], v[164:167], v[194:197], v[116:119]
	v_mfma_f32_16x16x32_bf16 v[112:115], v[190:193], v[194:197], v[112:115]
	ds_read_b128 v[194:197], v175 offset:43008
	s_waitcnt lgkmcnt(3)
	v_mfma_f32_16x16x32_bf16 v[8:11], v[190:193], v[4:7], v[8:11]
	s_waitcnt vmcnt(11)
	v_cvt_pk_bf16_f32 v29, v98, v99
	v_cvt_pk_bf16_f32 v28, v96, v97
	ds_write_b64 v174, v[28:29] offset:8704
	v_mfma_f32_16x16x32_bf16 v[108:111], v[24:27], v[4:7], v[108:111]
	v_mfma_f32_16x16x32_bf16 v[104:107], v[160:163], v[4:7], v[104:107]
	v_mfma_f32_16x16x32_bf16 v[100:103], v[164:167], v[4:7], v[100:103]
	buffer_load_dwordx4 v[28:31], v173, s[0:3], s58 offen
	ds_read_b128 v[96:99], v175 offset:45056
	s_waitcnt lgkmcnt(3)
	v_mfma_f32_16x16x32_bf16 v[92:95], v[24:27], v[198:201], v[92:95]
	v_mfma_f32_16x16x32_bf16 v[88:91], v[160:163], v[198:201], v[88:91]
	v_mfma_f32_16x16x32_bf16 v[84:87], v[164:167], v[198:201], v[84:87]
	v_mfma_f32_16x16x32_bf16 v[80:83], v[190:193], v[198:201], v[80:83]
	ds_read_b128 v[198:201], v175 offset:47104
	s_waitcnt lgkmcnt(3)
	v_mfma_f32_16x16x32_bf16 v[0:3], v[190:193], v[194:197], v[0:3]
	s_waitcnt vmcnt(11)
	v_cvt_pk_bf16_f32 v5, v66, v67
	v_cvt_pk_bf16_f32 v4, v64, v65
	ds_write_b64 v174, v[4:5] offset:17408
	v_mfma_f32_16x16x32_bf16 v[76:79], v[24:27], v[194:197], v[76:79]
	v_mfma_f32_16x16x32_bf16 v[72:75], v[160:163], v[194:197], v[72:75]
	v_mfma_f32_16x16x32_bf16 v[68:71], v[164:167], v[194:197], v[68:71]
	buffer_load_dwordx4 v[4:7], v173, s[0:3], s57 offen
	ds_read_b128 v[64:67], v175 offset:33792
	s_waitcnt lgkmcnt(3)
	v_mfma_f32_16x16x32_bf16 v[60:63], v[24:27], v[96:99], v[60:63]
	v_mfma_f32_16x16x32_bf16 v[56:59], v[160:163], v[96:99], v[56:59]
	v_mfma_f32_16x16x32_bf16 v[52:55], v[164:167], v[96:99], v[52:55]
	v_mfma_f32_16x16x32_bf16 v[48:51], v[190:193], v[96:99], v[48:51]
	ds_read_b128 v[96:99], v175 offset:35840
	ds_read_b64_tr_b16 v[194:195], v178 offset:52224
	ds_read_b64_tr_b16 v[202:203], v178 offset:52256
	ds_read_b64_tr_b16 v[206:207], v178 offset:52288
	ds_read_b64_tr_b16 v[210:211], v178 offset:52320
	ds_read_b64_tr_b16 v[196:197], v179 offset:52224
	ds_read_b64_tr_b16 v[204:205], v179 offset:52256
	ds_read_b64_tr_b16 v[208:209], v179 offset:52288
	ds_read_b64_tr_b16 v[212:213], v179 offset:52320
	s_waitcnt lgkmcnt(11)
	v_mfma_f32_16x16x32_bf16 v[16:19], v[190:193], v[198:201], v[16:19]
	v_mfma_f32_16x16x32_bf16 v[44:47], v[24:27], v[198:201], v[44:47]
	s_waitcnt vmcnt(11)
	v_cvt_pk_bf16_f32 v25, v34, v35
	v_cvt_pk_bf16_f32 v24, v32, v33
	ds_write_b64 v174, v[24:25] offset:26112
	v_mfma_f32_16x16x32_bf16 v[40:43], v[160:163], v[198:201], v[40:43]
	v_mfma_f32_16x16x32_bf16 v[36:39], v[164:167], v[198:201], v[36:39]
	buffer_load_dwordx4 v[24:27], v173, s[0:3], s59 offen
	ds_read_b128 v[32:35], v175 offset:37888
	s_waitcnt lgkmcnt(5)
	v_mfma_f32_16x16x32_bf16 v[190:193], v[194:197], v[64:67], v[156:159]
	s_waitcnt lgkmcnt(4)
	v_mfma_f32_16x16x32_bf16 v[198:201], v[202:205], v[64:67], v[152:155]
	s_waitcnt lgkmcnt(3)
	v_mfma_f32_16x16x32_bf16 v[164:167], v[206:209], v[64:67], v[148:151]
	s_waitcnt lgkmcnt(2)
	v_mfma_f32_16x16x32_bf16 v[160:163], v[210:213], v[64:67], v[144:147]
	ds_read_b128 v[64:67], v175 offset:39936
	s_waitcnt vmcnt(11)
	v_cvt_pk_bf16_f32 v23, v22, v23
	v_cvt_pk_bf16_f32 v22, v20, v21
	v_mfma_f32_16x16x32_bf16 v[156:159], v[194:197], v[96:99], v[140:143]
	ds_write_b64 v174, v[22:23] offset:256
	v_mfma_f32_16x16x32_bf16 v[152:155], v[202:205], v[96:99], v[136:139]
	v_mfma_f32_16x16x32_bf16 v[148:151], v[206:209], v[96:99], v[132:135]
	v_mfma_f32_16x16x32_bf16 v[144:147], v[210:213], v[96:99], v[128:131]
	buffer_load_dwordx4 v[20:23], v173, s[16:19], s56 offen
	ds_read_b128 v[96:99], v175 offset:41984
	s_waitcnt lgkmcnt(3)
	v_mfma_f32_16x16x32_bf16 v[140:143], v[194:197], v[32:35], v[124:127]
	v_mfma_f32_16x16x32_bf16 v[136:139], v[202:205], v[32:35], v[120:123]
	v_mfma_f32_16x16x32_bf16 v[132:135], v[206:209], v[32:35], v[116:119]
	v_mfma_f32_16x16x32_bf16 v[128:131], v[210:213], v[32:35], v[112:115]
	ds_read_b128 v[32:35], v175 offset:44032
	s_waitcnt lgkmcnt(3)
	v_mfma_f32_16x16x32_bf16 v[116:119], v[206:209], v[64:67], v[100:103]
	s_waitcnt vmcnt(11)
	s_nop 1
	v_cvt_pk_bf16_f32 v101, v184, v185
	v_cvt_pk_bf16_f32 v100, v182, v183
	v_mfma_f32_16x16x32_bf16 v[124:127], v[194:197], v[64:67], v[108:111]
	ds_write_b64 v174, v[100:101] offset:8960
	v_mfma_f32_16x16x32_bf16 v[120:123], v[202:205], v[64:67], v[104:107]
	v_mfma_f32_16x16x32_bf16 v[112:115], v[210:213], v[64:67], v[8:11]
	s_nop 2
	buffer_load_dwordx4 v[8:11], v173, s[16:19], s58 offen
	ds_read_b128 v[64:67], v175 offset:46080
	s_waitcnt lgkmcnt(3)
	v_mfma_f32_16x16x32_bf16 v[108:111], v[194:197], v[96:99], v[92:95]
	v_mfma_f32_16x16x32_bf16 v[104:107], v[202:205], v[96:99], v[88:91]
	v_mfma_f32_16x16x32_bf16 v[100:103], v[206:209], v[96:99], v[84:87]
	v_mfma_f32_16x16x32_bf16 v[96:99], v[210:213], v[96:99], v[80:83]
	ds_read_b128 v[182:185], v175 offset:48128
	s_waitcnt lgkmcnt(3)
	v_mfma_f32_16x16x32_bf16 v[84:87], v[206:209], v[32:35], v[68:71]
	s_waitcnt vmcnt(11)
	s_nop 1
	v_cvt_pk_bf16_f32 v69, v170, v171
	v_cvt_pk_bf16_f32 v68, v168, v169
	v_mfma_f32_16x16x32_bf16 v[92:95], v[194:197], v[32:35], v[76:79]
	ds_write_b64 v174, v[68:69] offset:17664
	v_mfma_f32_16x16x32_bf16 v[88:91], v[202:205], v[32:35], v[72:75]
	v_mfma_f32_16x16x32_bf16 v[80:83], v[210:213], v[32:35], v[0:3]
	s_nop 2
	buffer_load_dwordx4 v[0:3], v173, s[16:19], s57 offen
	s_waitcnt lgkmcnt(2)
	v_mfma_f32_16x16x32_bf16 v[76:79], v[194:197], v[64:67], v[60:63]
	v_mfma_f32_16x16x32_bf16 v[72:75], v[202:205], v[64:67], v[56:59]
	v_mfma_f32_16x16x32_bf16 v[68:71], v[206:209], v[64:67], v[52:55]
	v_mfma_f32_16x16x32_bf16 v[64:67], v[210:213], v[64:67], v[48:51]
	s_waitcnt vmcnt(11)
	v_cvt_pk_bf16_f32 v33, v188, v189
	v_cvt_pk_bf16_f32 v32, v186, v187
	s_waitcnt lgkmcnt(1)
	v_mfma_f32_16x16x32_bf16 v[60:63], v[194:197], v[182:185], v[44:47]
	ds_write_b64 v174, v[32:33] offset:26368
	v_mfma_f32_16x16x32_bf16 v[56:59], v[202:205], v[182:185], v[40:43]
	v_mfma_f32_16x16x32_bf16 v[40:43], v[206:209], v[182:185], v[36:39]
	v_mfma_f32_16x16x32_bf16 v[32:35], v[210:213], v[182:185], v[16:19]
	s_nop 2
	buffer_load_dwordx4 v[16:19], v173, s[16:19], s59 offen
	s_waitcnt vmcnt(8)
	s_waitcnt lgkmcnt(0)
	s_barrier
; DI float sigmoidf_(float x) { return __builtin_amdgcn_rcpf(1.0f + __expf(-x)); }
	s_mov_b32 s100, 0x10000
	s_mov_b32 s101, 0
	v_mbcnt_lo_u32_b32 v38, -1, 0
	v_mbcnt_hi_u32_b32 v38, -1, v38
	s_ashr_i32 s39, s38, 31
	s_lshl_b64 s[0:1], s[38:39], 2
	v_ashrrev_i32_e32 v36, 1, v38
	v_and_or_b32 v38, v38, 15, s66
	s_add_u32 s0, s67, s0
	v_and_b32_e32 v36, -8, v36
	v_add_u32_e32 v170, s74, v38
	s_addc_u32 s1, s68, s1
	v_ashrrev_i32_e32 v37, 31, v36
	v_ashrrev_i32_e32 v171, 31, v170
	s_or_b64 s[14:15], s[38:39], s[24:25]
	v_lshlrev_b64 v[38:39], 11, v[170:171]
	v_lshl_add_u64 v[168:169], s[14:15], 0, v[36:37]
	v_lshl_add_u64 v[194:195], v[38:39], 0, v[168:169]
	v_lshlrev_b64 v[38:39], 1, v[194:195]
	v_lshl_add_u64 v[196:197], s[30:31], 0, v[38:39]
	v_lshl_add_u64 v[202:203], s[40:41], 0, v[38:39]
	v_mov_b32_e32 v230, v196
	v_mov_b32_e32 v231, v197
	global_load_dwordx4 v[182:185], v[196:197], off
	v_mov_b32_e32 v238, v202
	v_mov_b32_e32 v239, v203
	global_load_dwordx4 v[186:189], v[202:203], off
	v_lshl_add_u64 v[38:39], v[170:171], 2, s[34:35]
	v_mov_b32_e32 v236, v38
	v_mov_b32_e32 v237, v39
	global_load_dword v172, v[38:39], off
	global_load_dwordx4 v[224:227], v[230:231], off offset:64
	global_load_dwordx4 v[232:235], v[238:239], off offset:64
	v_lshl_add_u64 v[44:45], v[36:37], 2, s[0:1]
	global_load_dwordx4 v[52:55], v[44:45], off
	global_load_dwordx4 v[48:51], v[44:45], off offset:16
	v_mul_f32_e32 v36, 0xbfb8aa3b, v190
	v_mul_f32_e32 v37, 0xbfb8aa3b, v191
	v_mul_f32_e32 v38, 0xbfb8aa3b, v192
	v_mul_f32_e32 v39, 0xbfb8aa3b, v193
	v_mul_f32_e32 v46, 0xbfb8aa3b, v198
	v_mul_f32_e32 v47, 0xbfb8aa3b, v199
	v_mul_f32_e32 v171, 0xbfb8aa3b, v200
	v_mul_f32_e32 v190, 0xbfb8aa3b, v201
	v_exp_f32_e32 v36, v36
	v_exp_f32_e32 v37, v37
	v_exp_f32_e32 v38, v38
	v_exp_f32_e32 v39, v39
	v_exp_f32_e32 v46, v46
	v_exp_f32_e32 v47, v47
	v_exp_f32_e32 v171, v171
	v_exp_f32_e32 v190, v190
	v_add_f32_e32 v191, 1.0, v36
	v_add_f32_e32 v192, 1.0, v37
	v_add_f32_e32 v193, 1.0, v38
	v_add_f32_e32 v198, 1.0, v39
	v_add_f32_e32 v199, 1.0, v46
	v_add_f32_e32 v200, 1.0, v47
	v_add_f32_e32 v171, 1.0, v171
	v_add_f32_e32 v201, 1.0, v190
	v_rcp_f32_e32 v190, v191
	v_rcp_f32_e32 v191, v192
	v_rcp_f32_e32 v192, v193
	v_rcp_f32_e32 v193, v198
	v_rcp_f32_e32 v198, v199
	v_rcp_f32_e32 v199, v200
	v_rcp_f32_e32 v200, v171
	v_rcp_f32_e32 v201, v201
	v_lshl_add_u64 v[194:195], v[194:195], 2, s[28:29]
	global_load_dwordx4 v[36:39], v[44:45], off offset:144
	s_nop 0
	global_load_dwordx4 v[44:47], v[44:45], off offset:128
	v_mul_f32_e32 v164, 0xbfb8aa3b, v164
	v_mul_f32_e32 v165, 0xbfb8aa3b, v165
	v_mul_f32_e32 v166, 0xbfb8aa3b, v166
	v_mul_f32_e32 v167, 0xbfb8aa3b, v167
	v_mul_f32_e32 v162, 0xbfb8aa3b, v162
	v_mul_f32_e32 v163, 0xbfb8aa3b, v163
	v_mul_f32_e32 v160, 0xbfb8aa3b, v160
	v_mul_f32_e32 v161, 0xbfb8aa3b, v161
	v_exp_f32_e32 v164, v164
	v_exp_f32_e32 v165, v165
	v_exp_f32_e32 v166, v166
	v_exp_f32_e32 v167, v167
	v_exp_f32_e32 v162, v162
	v_exp_f32_e32 v163, v163
	v_exp_f32_e32 v160, v160
	v_exp_f32_e32 v161, v161
	v_add_f32_e32 v164, 1.0, v164
	v_add_f32_e32 v165, 1.0, v165
	v_add_f32_e32 v166, 1.0, v166
	v_add_f32_e32 v167, 1.0, v167
	v_add_f32_e32 v171, 1.0, v160
	v_rcp_f32_e32 v160, v164
	v_rcp_f32_e32 v164, v171
	v_mul_f32_e32 v156, 0xbfb8aa3b, v156
	v_mul_f32_e32 v157, 0xbfb8aa3b, v157
	v_mul_f32_e32 v158, 0xbfb8aa3b, v158
	v_mul_f32_e32 v159, 0xbfb8aa3b, v159
	v_mul_f32_e32 v152, 0xbfb8aa3b, v152
	v_mul_f32_e32 v153, 0xbfb8aa3b, v153
	v_mul_f32_e32 v154, 0xbfb8aa3b, v154
	v_mul_f32_e32 v155, 0xbfb8aa3b, v155
	v_exp_f32_e32 v156, v156
	v_exp_f32_e32 v157, v157
	v_exp_f32_e32 v158, v158
	v_exp_f32_e32 v159, v159
	v_exp_f32_e32 v152, v152
	v_exp_f32_e32 v153, v153
	v_exp_f32_e32 v154, v154
	v_exp_f32_e32 v155, v155
	v_add_f32_e32 v156, 1.0, v156
	s_waitcnt vmcnt(8)
	v_lshlrev_b32_e32 v204, 16, v182
	v_and_b32_e32 v205, 0xffff0000, v182
	s_waitcnt vmcnt(7)
	v_lshlrev_b32_e32 v206, 16, v186
	v_and_b32_e32 v207, 0xffff0000, v186
	v_lshlrev_b32_e32 v208, 16, v183
	v_and_b32_e32 v209, 0xffff0000, v183
	v_lshlrev_b32_e32 v182, 16, v187
	v_and_b32_e32 v183, 0xffff0000, v187
	v_lshlrev_b32_e32 v186, 16, v184
	v_and_b32_e32 v187, 0xffff0000, v184
	v_lshlrev_b32_e32 v210, 16, v188
	v_and_b32_e32 v211, 0xffff0000, v188
	v_lshlrev_b32_e32 v212, 16, v185
	v_and_b32_e32 v213, 0xffff0000, v185
	v_lshlrev_b32_e32 v184, 16, v189
	v_and_b32_e32 v185, 0xffff0000, v189
	v_pk_mul_f32 v[188:189], v[190:191], v[206:207]
	v_pk_mul_f32 v[182:183], v[192:193], v[182:183]
	v_pk_mul_f32 v[190:191], v[198:199], v[210:211]
	v_pk_mul_f32 v[184:185], v[200:201], v[184:185]
	s_waitcnt vmcnt(6)
	v_pk_mul_f32 v[188:189], v[172:173], v[188:189] op_sel_hi:[0,1]
	v_pk_mul_f32 v[192:193], v[172:173], v[182:183] op_sel_hi:[0,1]
	v_pk_mul_f32 v[190:191], v[172:173], v[190:191] op_sel_hi:[0,1]
	v_pk_mul_f32 v[198:199], v[172:173], v[184:185] op_sel_hi:[0,1]
	s_waitcnt vmcnt(3)
	v_pk_fma_f32 v[182:183], v[52:53], v[188:189], v[204:205]
	v_pk_fma_f32 v[184:185], v[54:55], v[192:193], v[208:209]
	s_waitcnt vmcnt(2)
	v_pk_fma_f32 v[186:187], v[48:49], v[190:191], v[186:187]
	v_pk_fma_f32 v[188:189], v[50:51], v[198:199], v[212:213]
	global_store_dwordx4 v[194:195], v[182:185], off
	global_store_dwordx4 v[194:195], v[186:189], off offset:16
	v_lshl_add_u64 v[230:231], v[230:231], 0, s[100:101]
	global_load_dwordx4 v[216:219], v[230:231], off
	v_lshl_add_u64 v[238:239], v[238:239], 0, s[100:101]
	global_load_dwordx4 v[220:223], v[238:239], off
	global_load_dword v228, v[236:237], off offset:64
	s_nop 0
	v_add_f32_e32 v193, 1.0, v162
	v_add_f32_e32 v196, 1.0, v163
	v_add_f32_e32 v192, 1.0, v161
	v_rcp_f32_e32 v161, v165
	v_rcp_f32_e32 v162, v166
	v_rcp_f32_e32 v163, v167
	v_rcp_f32_e32 v166, v193
	v_rcp_f32_e32 v167, v196
	v_rcp_f32_e32 v165, v192
	v_add_u32_e32 v190, 16, v170
	v_ashrrev_i32_e32 v191, 31, v190
	v_lshlrev_b64 v[192:193], 11, v[190:191]
	v_lshl_add_u64 v[192:193], v[192:193], 0, v[168:169]
	v_lshlrev_b64 v[196:197], 1, v[192:193]
	v_lshl_add_u64 v[198:199], s[30:31], 0, v[196:197]
	v_add_f32_e32 v157, 1.0, v157
	v_add_f32_e32 v158, 1.0, v158
	v_add_f32_e32 v159, 1.0, v159
	v_add_f32_e32 v171, 1.0, v153
	v_rcp_f32_e32 v153, v157
	v_rcp_f32_e32 v157, v171
	v_mul_f32_e32 v148, 0xbfb8aa3b, v148
	v_mul_f32_e32 v149, 0xbfb8aa3b, v149
	v_mul_f32_e32 v150, 0xbfb8aa3b, v150
	v_mul_f32_e32 v151, 0xbfb8aa3b, v151
	v_mul_f32_e32 v144, 0xbfb8aa3b, v144
	v_mul_f32_e32 v145, 0xbfb8aa3b, v145
	v_mul_f32_e32 v146, 0xbfb8aa3b, v146
	v_mul_f32_e32 v147, 0xbfb8aa3b, v147
	v_exp_f32_e32 v148, v148
	v_exp_f32_e32 v149, v149
	v_exp_f32_e32 v150, v150
	v_exp_f32_e32 v151, v151
	v_exp_f32_e32 v144, v144
	v_exp_f32_e32 v145, v145
	v_exp_f32_e32 v146, v146
	v_exp_f32_e32 v147, v147
	v_add_f32_e32 v148, 1.0, v148
	v_add_f32_e32 v149, 1.0, v149
	v_add_f32_e32 v150, 1.0, v150
	v_add_f32_e32 v151, 1.0, v151
	v_mul_f32_e32 v140, 0xbfb8aa3b, v140
	v_mul_f32_e32 v141, 0xbfb8aa3b, v141
	v_mul_f32_e32 v142, 0xbfb8aa3b, v142
	v_mul_f32_e32 v143, 0xbfb8aa3b, v143
	v_mul_f32_e32 v136, 0xbfb8aa3b, v136
	v_mul_f32_e32 v137, 0xbfb8aa3b, v137
	v_mul_f32_e32 v138, 0xbfb8aa3b, v138
	v_mul_f32_e32 v139, 0xbfb8aa3b, v139
	v_exp_f32_e32 v140, v140
	v_exp_f32_e32 v141, v141
	v_exp_f32_e32 v142, v142
	v_exp_f32_e32 v143, v143
	v_exp_f32_e32 v136, v136
	v_exp_f32_e32 v137, v137
	v_exp_f32_e32 v138, v138
	v_exp_f32_e32 v139, v139
	v_add_f32_e32 v140, 1.0, v140
	v_add_f32_e32 v141, 1.0, v141
	v_add_f32_e32 v142, 1.0, v142
	v_add_f32_e32 v143, 1.0, v143
	v_mul_f32_e32 v132, 0xbfb8aa3b, v132
	v_mul_f32_e32 v133, 0xbfb8aa3b, v133
	v_mul_f32_e32 v134, 0xbfb8aa3b, v134
	v_mul_f32_e32 v135, 0xbfb8aa3b, v135
	v_mul_f32_e32 v128, 0xbfb8aa3b, v128
	v_mul_f32_e32 v129, 0xbfb8aa3b, v129
	v_mul_f32_e32 v130, 0xbfb8aa3b, v130
	v_mul_f32_e32 v131, 0xbfb8aa3b, v131
	v_exp_f32_e32 v132, v132
	v_exp_f32_e32 v133, v133
	v_exp_f32_e32 v134, v134
	v_exp_f32_e32 v135, v135
	v_exp_f32_e32 v128, v128
	v_exp_f32_e32 v129, v129
	v_exp_f32_e32 v130, v130
	v_exp_f32_e32 v131, v131
	v_add_f32_e32 v132, 1.0, v132
	s_waitcnt vmcnt(5)
	v_lshlrev_b32_e32 v200, 16, v224
	s_waitcnt vmcnt(5)
	v_lshlrev_b32_e32 v202, 16, v232
	v_and_b32_e32 v203, 0xffff0000, v232
	v_lshlrev_b32_e32 v186, 16, v233
	v_and_b32_e32 v187, 0xffff0000, v233
	v_lshlrev_b32_e32 v206, 16, v234
	v_and_b32_e32 v207, 0xffff0000, v234
	v_lshlrev_b32_e32 v188, 16, v235
	v_and_b32_e32 v189, 0xffff0000, v235
	v_pk_mul_f32 v[160:161], v[160:161], v[202:203]
	v_pk_mul_f32 v[162:163], v[162:163], v[186:187]
	v_pk_mul_f32 v[166:167], v[166:167], v[188:189]
	v_and_b32_e32 v201, 0xffff0000, v224
	v_lshlrev_b32_e32 v182, 16, v225
	v_and_b32_e32 v183, 0xffff0000, v225
	v_lshlrev_b32_e32 v204, 16, v226
	v_and_b32_e32 v205, 0xffff0000, v226
	v_lshlrev_b32_e32 v184, 16, v227
	v_and_b32_e32 v185, 0xffff0000, v227
	v_pk_mul_f32 v[164:165], v[164:165], v[206:207]
	v_pk_mul_f32 v[160:161], v[172:173], v[160:161] op_sel_hi:[0,1]
	v_pk_mul_f32 v[162:163], v[172:173], v[162:163] op_sel_hi:[0,1]
	v_pk_mul_f32 v[166:167], v[172:173], v[166:167] op_sel_hi:[0,1]
	v_pk_mul_f32 v[164:165], v[172:173], v[164:165] op_sel_hi:[0,1]
	v_pk_fma_f32 v[160:161], v[44:45], v[160:161], v[200:201]
	v_pk_fma_f32 v[162:163], v[46:47], v[162:163], v[182:183]
	v_pk_fma_f32 v[166:167], v[38:39], v[166:167], v[184:185]
	v_pk_fma_f32 v[164:165], v[36:37], v[164:165], v[204:205]
	global_store_dwordx4 v[194:195], v[160:163], off offset:128
	global_store_dwordx4 v[194:195], v[164:167], off offset:144
	global_load_dwordx4 v[224:227], v[230:231], off offset:64
	global_load_dwordx4 v[232:235], v[238:239], off offset:64
	v_lshl_add_u64 v[160:161], v[190:191], 2, s[34:35]
	v_lshl_add_u64 v[166:167], s[40:41], 0, v[196:197]
	v_add_f32_e32 v172, 1.0, v154
	v_add_f32_e32 v161, 1.0, v152
	v_add_f32_e32 v186, 1.0, v155
	v_rcp_f32_e32 v152, v156
	v_rcp_f32_e32 v154, v158
	v_rcp_f32_e32 v155, v159
	v_rcp_f32_e32 v156, v161
	v_rcp_f32_e32 v158, v172
	v_rcp_f32_e32 v159, v186
	v_lshl_add_u64 v[186:187], v[192:193], 2, s[28:29]
	v_add_f32_e32 v133, 1.0, v133
	v_add_f32_e32 v134, 1.0, v134
	v_add_f32_e32 v135, 1.0, v135
	v_mul_f32_e32 v124, 0xbfb8aa3b, v124
	v_mul_f32_e32 v125, 0xbfb8aa3b, v125
	v_mul_f32_e32 v126, 0xbfb8aa3b, v126
	v_mul_f32_e32 v127, 0xbfb8aa3b, v127
	v_mul_f32_e32 v120, 0xbfb8aa3b, v120
	v_mul_f32_e32 v121, 0xbfb8aa3b, v121
	v_mul_f32_e32 v122, 0xbfb8aa3b, v122
	v_mul_f32_e32 v123, 0xbfb8aa3b, v123
	v_exp_f32_e32 v124, v124
	v_exp_f32_e32 v125, v125
	v_exp_f32_e32 v126, v126
	v_exp_f32_e32 v127, v127
	v_exp_f32_e32 v120, v120
	v_exp_f32_e32 v121, v121
	v_exp_f32_e32 v122, v122
	v_exp_f32_e32 v123, v123
	v_add_f32_e32 v124, 1.0, v124
	v_add_f32_e32 v125, 1.0, v125
	v_add_f32_e32 v126, 1.0, v126
	v_add_f32_e32 v127, 1.0, v127
	v_mul_f32_e32 v116, 0xbfb8aa3b, v116
	v_mul_f32_e32 v117, 0xbfb8aa3b, v117
	v_mul_f32_e32 v118, 0xbfb8aa3b, v118
	v_mul_f32_e32 v119, 0xbfb8aa3b, v119
	v_mul_f32_e32 v112, 0xbfb8aa3b, v112
	v_mul_f32_e32 v113, 0xbfb8aa3b, v113
	v_mul_f32_e32 v114, 0xbfb8aa3b, v114
	v_mul_f32_e32 v115, 0xbfb8aa3b, v115
	v_exp_f32_e32 v116, v116
	v_exp_f32_e32 v117, v117
	v_exp_f32_e32 v118, v118
	v_exp_f32_e32 v119, v119
	v_exp_f32_e32 v112, v112
	v_exp_f32_e32 v113, v113
	v_exp_f32_e32 v114, v114
	v_exp_f32_e32 v115, v115
	v_add_f32_e32 v116, 1.0, v116
	v_add_f32_e32 v117, 1.0, v117
	v_add_f32_e32 v118, 1.0, v118
	v_add_f32_e32 v119, 1.0, v119
	v_mul_f32_e32 v108, 0xbfb8aa3b, v108
	v_mul_f32_e32 v109, 0xbfb8aa3b, v109
	v_mul_f32_e32 v110, 0xbfb8aa3b, v110
	v_mul_f32_e32 v111, 0xbfb8aa3b, v111
	v_mul_f32_e32 v104, 0xbfb8aa3b, v104
	v_mul_f32_e32 v105, 0xbfb8aa3b, v105
	v_mul_f32_e32 v106, 0xbfb8aa3b, v106
	v_mul_f32_e32 v107, 0xbfb8aa3b, v107
	v_exp_f32_e32 v108, v108
	v_exp_f32_e32 v109, v109
	v_exp_f32_e32 v110, v110
	v_exp_f32_e32 v111, v111
	v_exp_f32_e32 v104, v104
	v_exp_f32_e32 v105, v105
	v_exp_f32_e32 v106, v106
	v_exp_f32_e32 v107, v107
	v_add_f32_e32 v108, 1.0, v108
	v_add_f32_e32 v109, 1.0, v109
	v_add_f32_e32 v110, 1.0, v110
	v_add_f32_e32 v111, 1.0, v111
	v_mul_f32_e32 v100, 0xbfb8aa3b, v100
	v_mul_f32_e32 v101, 0xbfb8aa3b, v101
	s_waitcnt vmcnt(6)
	v_lshlrev_b32_e32 v188, 16, v216
	v_and_b32_e32 v189, 0xffff0000, v216
	v_lshlrev_b32_e32 v162, 16, v217
	s_waitcnt vmcnt(5)
	v_lshlrev_b32_e32 v190, 16, v220
	v_and_b32_e32 v191, 0xffff0000, v220
	v_lshlrev_b32_e32 v182, 16, v221
	v_and_b32_e32 v183, 0xffff0000, v221
	v_lshlrev_b32_e32 v194, 16, v222
	v_and_b32_e32 v195, 0xffff0000, v222
	v_lshlrev_b32_e32 v184, 16, v223
	v_and_b32_e32 v185, 0xffff0000, v223
	v_pk_mul_f32 v[152:153], v[152:153], v[190:191]
	v_pk_mul_f32 v[154:155], v[154:155], v[182:183]
	v_and_b32_e32 v163, 0xffff0000, v217
	v_pk_mul_f32 v[156:157], v[156:157], v[194:195]
	v_pk_mul_f32 v[158:159], v[158:159], v[184:185]
	s_waitcnt vmcnt(4)
	v_pk_mul_f32 v[152:153], v[228:229], v[152:153] op_sel_hi:[0,1]
	v_pk_mul_f32 v[154:155], v[228:229], v[154:155] op_sel_hi:[0,1]
	v_lshlrev_b32_e32 v192, 16, v218
	v_and_b32_e32 v193, 0xffff0000, v218
	v_lshlrev_b32_e32 v164, 16, v219
	v_and_b32_e32 v165, 0xffff0000, v219
	v_pk_mul_f32 v[156:157], v[228:229], v[156:157] op_sel_hi:[0,1]
	v_pk_mul_f32 v[158:159], v[228:229], v[158:159] op_sel_hi:[0,1]
	v_pk_fma_f32 v[152:153], v[52:53], v[152:153], v[188:189]
	v_pk_fma_f32 v[154:155], v[54:55], v[154:155], v[162:163]
	v_pk_fma_f32 v[156:157], v[48:49], v[156:157], v[192:193]
	v_pk_fma_f32 v[158:159], v[50:51], v[158:159], v[164:165]
	global_store_dwordx4 v[186:187], v[152:155], off
	global_store_dwordx4 v[186:187], v[156:159], off offset:16
	v_lshl_add_u64 v[238:239], v[238:239], 0, s[100:101]
	global_load_dwordx4 v[220:223], v[238:239], off
	v_lshl_add_u64 v[230:231], v[230:231], 0, s[100:101]
	global_load_dwordx4 v[216:219], v[230:231], off
	global_load_dword v214, v[236:237], off offset:128
	s_nop 0
	v_add_f32_e32 v161, 1.0, v144
	v_add_f32_e32 v164, 1.0, v145
	v_add_f32_e32 v165, 1.0, v146
	v_add_f32_e32 v166, 1.0, v147
	v_rcp_f32_e32 v144, v148
	v_rcp_f32_e32 v145, v149
	v_rcp_f32_e32 v146, v150
	v_rcp_f32_e32 v147, v151
	v_rcp_f32_e32 v148, v161
	v_rcp_f32_e32 v149, v164
	v_rcp_f32_e32 v150, v165
	v_rcp_f32_e32 v151, v166
	v_add_u32_e32 v162, 32, v170
	v_ashrrev_i32_e32 v163, 31, v162
	v_lshlrev_b64 v[164:165], 11, v[162:163]
	v_lshl_add_u64 v[164:165], v[164:165], 0, v[168:169]
	v_lshlrev_b64 v[166:167], 1, v[164:165]
	v_lshl_add_u64 v[182:183], s[30:31], 0, v[166:167]
	v_mul_f32_e32 v102, 0xbfb8aa3b, v102
	v_mul_f32_e32 v103, 0xbfb8aa3b, v103
	v_mul_f32_e32 v96, 0xbfb8aa3b, v96
	v_mul_f32_e32 v97, 0xbfb8aa3b, v97
	v_mul_f32_e32 v98, 0xbfb8aa3b, v98
	v_mul_f32_e32 v99, 0xbfb8aa3b, v99
	v_exp_f32_e32 v100, v100
	v_exp_f32_e32 v101, v101
	v_exp_f32_e32 v102, v102
	v_exp_f32_e32 v103, v103
	v_exp_f32_e32 v96, v96
	v_exp_f32_e32 v97, v97
	v_exp_f32_e32 v98, v98
	v_exp_f32_e32 v99, v99
	v_add_f32_e32 v100, 1.0, v100
	v_add_f32_e32 v101, 1.0, v101
	v_add_f32_e32 v102, 1.0, v102
	v_add_f32_e32 v103, 1.0, v103
	v_mul_f32_e32 v92, 0xbfb8aa3b, v92
	v_mul_f32_e32 v93, 0xbfb8aa3b, v93
	v_mul_f32_e32 v94, 0xbfb8aa3b, v94
	v_mul_f32_e32 v95, 0xbfb8aa3b, v95
	v_mul_f32_e32 v88, 0xbfb8aa3b, v88
	v_mul_f32_e32 v89, 0xbfb8aa3b, v89
	v_mul_f32_e32 v90, 0xbfb8aa3b, v90
	v_mul_f32_e32 v91, 0xbfb8aa3b, v91
	v_exp_f32_e32 v92, v92
	v_exp_f32_e32 v93, v93
	v_exp_f32_e32 v94, v94
	v_exp_f32_e32 v95, v95
	v_exp_f32_e32 v88, v88
	v_exp_f32_e32 v89, v89
	v_exp_f32_e32 v90, v90
	v_exp_f32_e32 v91, v91
	v_add_f32_e32 v92, 1.0, v92
	v_add_f32_e32 v93, 1.0, v93
	v_add_f32_e32 v94, 1.0, v94
	v_add_f32_e32 v95, 1.0, v95
	v_mul_f32_e32 v84, 0xbfb8aa3b, v84
	v_mul_f32_e32 v85, 0xbfb8aa3b, v85
	v_mul_f32_e32 v86, 0xbfb8aa3b, v86
	v_mul_f32_e32 v87, 0xbfb8aa3b, v87
	v_mul_f32_e32 v80, 0xbfb8aa3b, v80
	v_mul_f32_e32 v81, 0xbfb8aa3b, v81
	v_mul_f32_e32 v82, 0xbfb8aa3b, v82
	v_mul_f32_e32 v83, 0xbfb8aa3b, v83
	v_exp_f32_e32 v84, v84
	v_exp_f32_e32 v85, v85
	v_exp_f32_e32 v86, v86
	v_exp_f32_e32 v87, v87
	v_exp_f32_e32 v80, v80
	v_exp_f32_e32 v81, v81
	v_exp_f32_e32 v82, v82
	v_exp_f32_e32 v83, v83
	v_add_f32_e32 v84, 1.0, v84
	v_add_f32_e32 v85, 1.0, v85
	v_add_f32_e32 v86, 1.0, v86
	v_add_f32_e32 v87, 1.0, v87
	v_mul_f32_e32 v76, 0xbfb8aa3b, v76
	v_mul_f32_e32 v77, 0xbfb8aa3b, v77
	s_waitcnt vmcnt(6)
	v_lshlrev_b32_e32 v184, 16, v224
	s_waitcnt vmcnt(5)
	v_lshlrev_b32_e32 v188, 16, v232
	v_and_b32_e32 v189, 0xffff0000, v232
	v_lshlrev_b32_e32 v156, 16, v233
	v_and_b32_e32 v157, 0xffff0000, v233
	v_lshlrev_b32_e32 v192, 16, v234
	v_and_b32_e32 v193, 0xffff0000, v234
	v_lshlrev_b32_e32 v158, 16, v235
	v_and_b32_e32 v159, 0xffff0000, v235
	v_pk_mul_f32 v[144:145], v[144:145], v[188:189]
	v_pk_mul_f32 v[146:147], v[146:147], v[156:157]
	v_and_b32_e32 v185, 0xffff0000, v224
	v_lshlrev_b32_e32 v152, 16, v225
	v_and_b32_e32 v153, 0xffff0000, v225
	v_pk_mul_f32 v[148:149], v[148:149], v[192:193]
	v_pk_mul_f32 v[150:151], v[150:151], v[158:159]
	v_pk_mul_f32 v[144:145], v[228:229], v[144:145] op_sel_hi:[0,1]
	v_pk_mul_f32 v[146:147], v[228:229], v[146:147] op_sel_hi:[0,1]
	v_lshlrev_b32_e32 v190, 16, v226
	v_and_b32_e32 v191, 0xffff0000, v226
	v_lshlrev_b32_e32 v154, 16, v227
	v_and_b32_e32 v155, 0xffff0000, v227
	v_pk_mul_f32 v[148:149], v[228:229], v[148:149] op_sel_hi:[0,1]
	v_pk_mul_f32 v[150:151], v[228:229], v[150:151] op_sel_hi:[0,1]
	v_pk_fma_f32 v[144:145], v[44:45], v[144:145], v[184:185]
	v_pk_fma_f32 v[146:147], v[46:47], v[146:147], v[152:153]
	v_pk_fma_f32 v[148:149], v[36:37], v[148:149], v[190:191]
	v_pk_fma_f32 v[150:151], v[38:39], v[150:151], v[154:155]
	global_store_dwordx4 v[186:187], v[144:147], off offset:128
	global_store_dwordx4 v[186:187], v[148:151], off offset:144
	v_lshl_add_u64 v[154:155], s[40:41], 0, v[166:167]
	global_load_dwordx4 v[224:227], v[230:231], off offset:64
	global_load_dwordx4 v[232:235], v[238:239], off offset:64
	v_lshl_add_u64 v[144:145], v[162:163], 2, s[34:35]
	v_add_f32_e32 v156, 1.0, v137
	v_add_f32_e32 v145, 1.0, v136
	v_add_f32_e32 v157, 1.0, v138
	v_add_f32_e32 v158, 1.0, v139
	v_rcp_f32_e32 v136, v140
	v_rcp_f32_e32 v137, v141
	v_rcp_f32_e32 v138, v142
	v_rcp_f32_e32 v139, v143
	v_rcp_f32_e32 v140, v145
	v_rcp_f32_e32 v141, v156
	v_rcp_f32_e32 v142, v157
	v_rcp_f32_e32 v143, v158
	v_lshl_add_u64 v[156:157], v[164:165], 2, s[28:29]
	v_mul_f32_e32 v78, 0xbfb8aa3b, v78
	v_mul_f32_e32 v79, 0xbfb8aa3b, v79
	v_mul_f32_e32 v72, 0xbfb8aa3b, v72
	v_mul_f32_e32 v73, 0xbfb8aa3b, v73
	v_mul_f32_e32 v74, 0xbfb8aa3b, v74
	v_mul_f32_e32 v75, 0xbfb8aa3b, v75
	v_exp_f32_e32 v76, v76
	v_exp_f32_e32 v77, v77
	v_exp_f32_e32 v78, v78
	v_exp_f32_e32 v79, v79
	v_exp_f32_e32 v72, v72
	v_exp_f32_e32 v73, v73
	v_exp_f32_e32 v74, v74
	v_exp_f32_e32 v75, v75
	v_add_f32_e32 v76, 1.0, v76
	v_add_f32_e32 v77, 1.0, v77
	v_add_f32_e32 v78, 1.0, v78
	v_add_f32_e32 v79, 1.0, v79
	v_mul_f32_e32 v68, 0xbfb8aa3b, v68
	v_mul_f32_e32 v69, 0xbfb8aa3b, v69
	v_mul_f32_e32 v70, 0xbfb8aa3b, v70
	v_mul_f32_e32 v71, 0xbfb8aa3b, v71
	v_mul_f32_e32 v64, 0xbfb8aa3b, v64
	v_mul_f32_e32 v65, 0xbfb8aa3b, v65
	v_mul_f32_e32 v66, 0xbfb8aa3b, v66
	v_mul_f32_e32 v67, 0xbfb8aa3b, v67
	v_exp_f32_e32 v68, v68
	v_exp_f32_e32 v69, v69
	v_exp_f32_e32 v70, v70
	v_exp_f32_e32 v71, v71
	v_exp_f32_e32 v64, v64
	v_exp_f32_e32 v65, v65
	v_exp_f32_e32 v66, v66
	v_exp_f32_e32 v67, v67
	v_add_f32_e32 v68, 1.0, v68
	v_add_f32_e32 v69, 1.0, v69
	v_add_f32_e32 v70, 1.0, v70
	v_add_f32_e32 v71, 1.0, v71
	v_mul_f32_e32 v60, 0xbfb8aa3b, v60
	v_mul_f32_e32 v61, 0xbfb8aa3b, v61
	v_mul_f32_e32 v62, 0xbfb8aa3b, v62
	v_mul_f32_e32 v63, 0xbfb8aa3b, v63
	v_mul_f32_e32 v56, 0xbfb8aa3b, v56
	v_mul_f32_e32 v57, 0xbfb8aa3b, v57
	v_mul_f32_e32 v58, 0xbfb8aa3b, v58
	v_mul_f32_e32 v59, 0xbfb8aa3b, v59
	v_exp_f32_e32 v60, v60
	v_exp_f32_e32 v61, v61
	v_exp_f32_e32 v62, v62
	v_exp_f32_e32 v63, v63
	v_exp_f32_e32 v56, v56
	v_exp_f32_e32 v57, v57
	v_exp_f32_e32 v58, v58
	v_exp_f32_e32 v59, v59
	v_add_f32_e32 v60, 1.0, v60
	v_add_f32_e32 v61, 1.0, v61
	v_add_f32_e32 v62, 1.0, v62
	v_add_f32_e32 v63, 1.0, v63
	v_mul_f32_e32 v40, 0xbfb8aa3b, v40
	v_mul_f32_e32 v41, 0xbfb8aa3b, v41
	v_mul_f32_e32 v42, 0xbfb8aa3b, v42
	v_mul_f32_e32 v43, 0xbfb8aa3b, v43
	v_mul_f32_e32 v32, 0xbfb8aa3b, v32
	s_waitcnt vmcnt(6)
	v_lshlrev_b32_e32 v160, 16, v220
	v_and_b32_e32 v161, 0xffff0000, v220
	v_lshlrev_b32_e32 v150, 16, v221
	v_and_b32_e32 v151, 0xffff0000, v221
	v_lshlrev_b32_e32 v164, 16, v222
	v_and_b32_e32 v165, 0xffff0000, v222
	v_lshlrev_b32_e32 v152, 16, v223
	v_and_b32_e32 v153, 0xffff0000, v223
	v_pk_mul_f32 v[136:137], v[136:137], v[160:161]
	v_pk_mul_f32 v[138:139], v[138:139], v[150:151]
	s_waitcnt vmcnt(5)
	v_lshlrev_b32_e32 v158, 16, v216
	v_and_b32_e32 v159, 0xffff0000, v216
	v_lshlrev_b32_e32 v146, 16, v217
	v_and_b32_e32 v147, 0xffff0000, v217
	v_pk_mul_f32 v[140:141], v[140:141], v[164:165]
	v_pk_mul_f32 v[142:143], v[142:143], v[152:153]
	s_waitcnt vmcnt(4)
	v_pk_mul_f32 v[136:137], v[214:215], v[136:137] op_sel_hi:[0,1]
	v_pk_mul_f32 v[138:139], v[214:215], v[138:139] op_sel_hi:[0,1]
	v_lshlrev_b32_e32 v162, 16, v218
	v_and_b32_e32 v163, 0xffff0000, v218
	v_lshlrev_b32_e32 v148, 16, v219
	v_and_b32_e32 v149, 0xffff0000, v219
	v_pk_mul_f32 v[140:141], v[214:215], v[140:141] op_sel_hi:[0,1]
	v_pk_mul_f32 v[142:143], v[214:215], v[142:143] op_sel_hi:[0,1]
	v_pk_fma_f32 v[136:137], v[52:53], v[136:137], v[158:159]
	v_pk_fma_f32 v[138:139], v[54:55], v[138:139], v[146:147]
	v_pk_fma_f32 v[140:141], v[48:49], v[140:141], v[162:163]
	v_pk_fma_f32 v[142:143], v[50:51], v[142:143], v[148:149]
	global_store_dwordx4 v[156:157], v[136:139], off
	global_store_dwordx4 v[156:157], v[140:143], off offset:16
	v_lshl_add_u64 v[238:239], v[238:239], 0, s[100:101]
	global_load_dwordx4 v[220:223], v[238:239], off
	v_lshl_add_u64 v[230:231], v[230:231], 0, s[100:101]
	global_load_dwordx4 v[216:219], v[230:231], off
	global_load_dword v228, v[236:237], off offset:192
	s_nop 0
	v_add_f32_e32 v145, 1.0, v128
	v_add_f32_e32 v148, 1.0, v129
	v_add_f32_e32 v149, 1.0, v130
	v_add_f32_e32 v150, 1.0, v131
	v_rcp_f32_e32 v128, v132
	v_rcp_f32_e32 v129, v133
	v_rcp_f32_e32 v130, v134
	v_rcp_f32_e32 v131, v135
	v_rcp_f32_e32 v132, v145
	v_rcp_f32_e32 v133, v148
	v_rcp_f32_e32 v134, v149
	v_rcp_f32_e32 v135, v150
	v_add_u32_e32 v146, 48, v170
	v_ashrrev_i32_e32 v147, 31, v146
	v_lshlrev_b64 v[148:149], 11, v[146:147]
	v_lshl_add_u64 v[148:149], v[148:149], 0, v[168:169]
	v_lshlrev_b64 v[150:151], 1, v[148:149]
	v_lshl_add_u64 v[152:153], s[30:31], 0, v[150:151]
	v_mul_f32_e32 v33, 0xbfb8aa3b, v33
	v_mul_f32_e32 v34, 0xbfb8aa3b, v34
	v_mul_f32_e32 v35, 0xbfb8aa3b, v35
	v_exp_f32_e32 v40, v40
	v_exp_f32_e32 v41, v41
	v_exp_f32_e32 v42, v42
	v_exp_f32_e32 v43, v43
	v_exp_f32_e32 v32, v32
	v_exp_f32_e32 v33, v33
	v_exp_f32_e32 v34, v34
	v_exp_f32_e32 v35, v35
	v_add_f32_e32 v40, 1.0, v40
	v_add_f32_e32 v41, 1.0, v41
	v_add_f32_e32 v42, 1.0, v42
	v_add_f32_e32 v43, 1.0, v43
	s_mov_b64 s[16:17], s[10:11]
	s_mov_b64 s[18:19], s[2:3]
	s_mov_b64 s[14:15], s[2:3]
	s_mov_b64 s[10:11], s[2:3]
	s_and_b64 vcc, exec, s[4:5]
	s_mov_b32 s74, s71
	s_mov_b32 s38, s36
	s_waitcnt vmcnt(6)
	v_lshlrev_b32_e32 v154, 16, v224
	s_waitcnt vmcnt(5)
	v_lshlrev_b32_e32 v158, 16, v232
	v_and_b32_e32 v159, 0xffff0000, v232
	v_lshlrev_b32_e32 v140, 16, v233
	v_and_b32_e32 v141, 0xffff0000, v233
	v_lshlrev_b32_e32 v162, 16, v234
	v_and_b32_e32 v163, 0xffff0000, v234
	v_lshlrev_b32_e32 v142, 16, v235
	v_and_b32_e32 v143, 0xffff0000, v235
	v_pk_mul_f32 v[128:129], v[128:129], v[158:159]
	v_pk_mul_f32 v[130:131], v[130:131], v[140:141]
	v_and_b32_e32 v155, 0xffff0000, v224
	v_lshlrev_b32_e32 v136, 16, v225
	v_and_b32_e32 v137, 0xffff0000, v225
	v_pk_mul_f32 v[132:133], v[132:133], v[162:163]
	v_pk_mul_f32 v[134:135], v[134:135], v[142:143]
	v_pk_mul_f32 v[128:129], v[214:215], v[128:129] op_sel_hi:[0,1]
	v_pk_mul_f32 v[130:131], v[214:215], v[130:131] op_sel_hi:[0,1]
	v_lshlrev_b32_e32 v160, 16, v226
	v_and_b32_e32 v161, 0xffff0000, v226
	v_lshlrev_b32_e32 v138, 16, v227
	v_and_b32_e32 v139, 0xffff0000, v227
	v_pk_mul_f32 v[132:133], v[214:215], v[132:133] op_sel_hi:[0,1]
	v_pk_mul_f32 v[134:135], v[214:215], v[134:135] op_sel_hi:[0,1]
	v_pk_fma_f32 v[128:129], v[44:45], v[128:129], v[154:155]
	v_pk_fma_f32 v[130:131], v[46:47], v[130:131], v[136:137]
	v_pk_fma_f32 v[132:133], v[36:37], v[132:133], v[160:161]
	v_pk_fma_f32 v[134:135], v[38:39], v[134:135], v[138:139]
	global_store_dwordx4 v[156:157], v[128:131], off offset:128
	global_store_dwordx4 v[156:157], v[132:135], off offset:144
	v_lshl_add_u64 v[138:139], s[40:41], 0, v[150:151]
	global_load_dwordx4 v[224:227], v[230:231], off offset:64
	global_load_dwordx4 v[232:235], v[238:239], off offset:64
	v_lshl_add_u64 v[128:129], v[146:147], 2, s[34:35]
	v_add_f32_e32 v140, 1.0, v121
	v_add_f32_e32 v129, 1.0, v120
	v_add_f32_e32 v141, 1.0, v122
	v_add_f32_e32 v142, 1.0, v123
	v_rcp_f32_e32 v120, v124
	v_rcp_f32_e32 v121, v125
	v_rcp_f32_e32 v122, v126
	v_rcp_f32_e32 v123, v127
	v_rcp_f32_e32 v124, v129
	v_rcp_f32_e32 v125, v140
	v_rcp_f32_e32 v126, v141
	v_rcp_f32_e32 v127, v142
	v_lshl_add_u64 v[140:141], v[148:149], 2, s[28:29]
	s_waitcnt vmcnt(6)
	v_lshlrev_b32_e32 v144, 16, v220
	v_and_b32_e32 v145, 0xffff0000, v220
	v_lshlrev_b32_e32 v134, 16, v221
	v_and_b32_e32 v135, 0xffff0000, v221
	v_lshlrev_b32_e32 v148, 16, v222
	v_and_b32_e32 v149, 0xffff0000, v222
	v_lshlrev_b32_e32 v136, 16, v223
	v_and_b32_e32 v137, 0xffff0000, v223
	v_pk_mul_f32 v[120:121], v[120:121], v[144:145]
	v_pk_mul_f32 v[122:123], v[122:123], v[134:135]
	s_waitcnt vmcnt(5)
	v_lshlrev_b32_e32 v142, 16, v216
	v_and_b32_e32 v143, 0xffff0000, v216
	v_lshlrev_b32_e32 v130, 16, v217
	v_and_b32_e32 v131, 0xffff0000, v217
	v_pk_mul_f32 v[124:125], v[124:125], v[148:149]
	v_pk_mul_f32 v[126:127], v[126:127], v[136:137]
	s_waitcnt vmcnt(4)
	v_pk_mul_f32 v[120:121], v[228:229], v[120:121] op_sel_hi:[0,1]
	v_pk_mul_f32 v[122:123], v[228:229], v[122:123] op_sel_hi:[0,1]
	v_lshlrev_b32_e32 v146, 16, v218
	v_and_b32_e32 v147, 0xffff0000, v218
	v_lshlrev_b32_e32 v132, 16, v219
	v_and_b32_e32 v133, 0xffff0000, v219
	v_pk_mul_f32 v[124:125], v[228:229], v[124:125] op_sel_hi:[0,1]
	v_pk_mul_f32 v[126:127], v[228:229], v[126:127] op_sel_hi:[0,1]
	v_pk_fma_f32 v[120:121], v[52:53], v[120:121], v[142:143]
	v_pk_fma_f32 v[122:123], v[54:55], v[122:123], v[130:131]
	v_pk_fma_f32 v[124:125], v[48:49], v[124:125], v[146:147]
	v_pk_fma_f32 v[126:127], v[50:51], v[126:127], v[132:133]
	global_store_dwordx4 v[140:141], v[120:123], off
	global_store_dwordx4 v[140:141], v[124:127], off offset:16
	v_lshl_add_u64 v[238:239], v[238:239], 0, s[100:101]
	global_load_dwordx4 v[220:223], v[238:239], off
	v_lshl_add_u64 v[230:231], v[230:231], 0, s[100:101]
	global_load_dwordx4 v[216:219], v[230:231], off
	global_load_dword v214, v[236:237], off offset:256
	s_nop 0
	v_add_f32_e32 v129, 1.0, v112
	v_add_f32_e32 v132, 1.0, v113
	v_add_f32_e32 v133, 1.0, v114
	v_add_f32_e32 v134, 1.0, v115
	v_rcp_f32_e32 v112, v116
	v_rcp_f32_e32 v113, v117
	v_rcp_f32_e32 v114, v118
	v_rcp_f32_e32 v115, v119
	v_rcp_f32_e32 v116, v129
	v_rcp_f32_e32 v117, v132
	v_rcp_f32_e32 v118, v133
	v_rcp_f32_e32 v119, v134
	v_add_u32_e32 v130, 64, v170
	v_ashrrev_i32_e32 v131, 31, v130
	v_lshlrev_b64 v[132:133], 11, v[130:131]
	v_lshl_add_u64 v[132:133], v[132:133], 0, v[168:169]
	v_lshlrev_b64 v[134:135], 1, v[132:133]
	v_lshl_add_u64 v[136:137], s[30:31], 0, v[134:135]
	s_waitcnt vmcnt(6)
	v_lshlrev_b32_e32 v138, 16, v224
	s_waitcnt vmcnt(5)
	v_lshlrev_b32_e32 v142, 16, v232
	v_and_b32_e32 v143, 0xffff0000, v232
	v_lshlrev_b32_e32 v124, 16, v233
	v_and_b32_e32 v125, 0xffff0000, v233
	v_lshlrev_b32_e32 v146, 16, v234
	v_and_b32_e32 v147, 0xffff0000, v234
	v_lshlrev_b32_e32 v126, 16, v235
	v_and_b32_e32 v127, 0xffff0000, v235
	v_pk_mul_f32 v[112:113], v[112:113], v[142:143]
	v_pk_mul_f32 v[114:115], v[114:115], v[124:125]
	v_and_b32_e32 v139, 0xffff0000, v224
	v_lshlrev_b32_e32 v120, 16, v225
	v_and_b32_e32 v121, 0xffff0000, v225
	v_pk_mul_f32 v[116:117], v[116:117], v[146:147]
	v_pk_mul_f32 v[118:119], v[118:119], v[126:127]
	v_pk_mul_f32 v[112:113], v[228:229], v[112:113] op_sel_hi:[0,1]
	v_pk_mul_f32 v[114:115], v[228:229], v[114:115] op_sel_hi:[0,1]
	v_lshlrev_b32_e32 v144, 16, v226
	v_and_b32_e32 v145, 0xffff0000, v226
	v_lshlrev_b32_e32 v122, 16, v227
	v_and_b32_e32 v123, 0xffff0000, v227
	v_pk_mul_f32 v[116:117], v[228:229], v[116:117] op_sel_hi:[0,1]
	v_pk_mul_f32 v[118:119], v[228:229], v[118:119] op_sel_hi:[0,1]
	v_pk_fma_f32 v[112:113], v[44:45], v[112:113], v[138:139]
	v_pk_fma_f32 v[114:115], v[46:47], v[114:115], v[120:121]
	v_pk_fma_f32 v[116:117], v[36:37], v[116:117], v[144:145]
	v_pk_fma_f32 v[118:119], v[38:39], v[118:119], v[122:123]
	global_store_dwordx4 v[140:141], v[112:115], off offset:128
	global_store_dwordx4 v[140:141], v[116:119], off offset:144
	v_lshl_add_u64 v[122:123], s[40:41], 0, v[134:135]
	global_load_dwordx4 v[224:227], v[230:231], off offset:64
	global_load_dwordx4 v[232:235], v[238:239], off offset:64
	v_lshl_add_u64 v[112:113], v[130:131], 2, s[34:35]
	v_add_f32_e32 v124, 1.0, v105
	v_add_f32_e32 v113, 1.0, v104
	v_add_f32_e32 v125, 1.0, v106
	v_add_f32_e32 v126, 1.0, v107
	v_rcp_f32_e32 v104, v108
	v_rcp_f32_e32 v105, v109
	v_rcp_f32_e32 v106, v110
	v_rcp_f32_e32 v107, v111
	v_rcp_f32_e32 v108, v113
	v_rcp_f32_e32 v109, v124
	v_rcp_f32_e32 v110, v125
	v_rcp_f32_e32 v111, v126
	v_lshl_add_u64 v[124:125], v[132:133], 2, s[28:29]
	s_waitcnt vmcnt(6)
	v_lshlrev_b32_e32 v128, 16, v220
	v_and_b32_e32 v129, 0xffff0000, v220
	v_lshlrev_b32_e32 v118, 16, v221
	v_and_b32_e32 v119, 0xffff0000, v221
	v_lshlrev_b32_e32 v132, 16, v222
	v_and_b32_e32 v133, 0xffff0000, v222
	v_lshlrev_b32_e32 v120, 16, v223
	v_and_b32_e32 v121, 0xffff0000, v223
	v_pk_mul_f32 v[104:105], v[104:105], v[128:129]
	v_pk_mul_f32 v[106:107], v[106:107], v[118:119]
	s_waitcnt vmcnt(5)
	v_lshlrev_b32_e32 v126, 16, v216
	v_and_b32_e32 v127, 0xffff0000, v216
	v_lshlrev_b32_e32 v114, 16, v217
	v_and_b32_e32 v115, 0xffff0000, v217
	v_pk_mul_f32 v[108:109], v[108:109], v[132:133]
	v_pk_mul_f32 v[110:111], v[110:111], v[120:121]
	s_waitcnt vmcnt(4)
	v_pk_mul_f32 v[104:105], v[214:215], v[104:105] op_sel_hi:[0,1]
	v_pk_mul_f32 v[106:107], v[214:215], v[106:107] op_sel_hi:[0,1]
	v_lshlrev_b32_e32 v130, 16, v218
	v_and_b32_e32 v131, 0xffff0000, v218
	v_lshlrev_b32_e32 v116, 16, v219
	v_and_b32_e32 v117, 0xffff0000, v219
	v_pk_mul_f32 v[108:109], v[214:215], v[108:109] op_sel_hi:[0,1]
	v_pk_mul_f32 v[110:111], v[214:215], v[110:111] op_sel_hi:[0,1]
	v_pk_fma_f32 v[104:105], v[52:53], v[104:105], v[126:127]
	v_pk_fma_f32 v[106:107], v[54:55], v[106:107], v[114:115]
	v_pk_fma_f32 v[108:109], v[48:49], v[108:109], v[130:131]
	v_pk_fma_f32 v[110:111], v[50:51], v[110:111], v[116:117]
	global_store_dwordx4 v[124:125], v[104:107], off
	global_store_dwordx4 v[124:125], v[108:111], off offset:16
	v_lshl_add_u64 v[238:239], v[238:239], 0, s[100:101]
	global_load_dwordx4 v[220:223], v[238:239], off
	v_lshl_add_u64 v[230:231], v[230:231], 0, s[100:101]
	global_load_dwordx4 v[216:219], v[230:231], off
	global_load_dword v228, v[236:237], off offset:320
	s_nop 0
	v_add_f32_e32 v113, 1.0, v96
	v_add_f32_e32 v116, 1.0, v97
	v_add_f32_e32 v117, 1.0, v98
	v_add_f32_e32 v118, 1.0, v99
	v_rcp_f32_e32 v96, v100
	v_rcp_f32_e32 v97, v101
	v_rcp_f32_e32 v98, v102
	v_rcp_f32_e32 v99, v103
	v_rcp_f32_e32 v100, v113
	v_rcp_f32_e32 v101, v116
	v_rcp_f32_e32 v102, v117
	v_rcp_f32_e32 v103, v118
	v_add_u32_e32 v114, 0x50, v170
	v_ashrrev_i32_e32 v115, 31, v114
	v_lshlrev_b64 v[116:117], 11, v[114:115]
	v_lshl_add_u64 v[116:117], v[116:117], 0, v[168:169]
	v_lshlrev_b64 v[118:119], 1, v[116:117]
	v_lshl_add_u64 v[120:121], s[30:31], 0, v[118:119]
	s_waitcnt vmcnt(6)
	v_lshlrev_b32_e32 v122, 16, v224
	s_waitcnt vmcnt(5)
	v_lshlrev_b32_e32 v126, 16, v232
	v_and_b32_e32 v127, 0xffff0000, v232
	v_lshlrev_b32_e32 v108, 16, v233
	v_and_b32_e32 v109, 0xffff0000, v233
	v_lshlrev_b32_e32 v130, 16, v234
	v_and_b32_e32 v131, 0xffff0000, v234
	v_lshlrev_b32_e32 v110, 16, v235
	v_and_b32_e32 v111, 0xffff0000, v235
	v_pk_mul_f32 v[96:97], v[96:97], v[126:127]
	v_pk_mul_f32 v[98:99], v[98:99], v[108:109]
	v_and_b32_e32 v123, 0xffff0000, v224
	v_lshlrev_b32_e32 v104, 16, v225
	v_and_b32_e32 v105, 0xffff0000, v225
	v_pk_mul_f32 v[100:101], v[100:101], v[130:131]
	v_pk_mul_f32 v[102:103], v[102:103], v[110:111]
	v_pk_mul_f32 v[96:97], v[214:215], v[96:97] op_sel_hi:[0,1]
	v_pk_mul_f32 v[98:99], v[214:215], v[98:99] op_sel_hi:[0,1]
	v_lshlrev_b32_e32 v128, 16, v226
	v_and_b32_e32 v129, 0xffff0000, v226
	v_lshlrev_b32_e32 v106, 16, v227
	v_and_b32_e32 v107, 0xffff0000, v227
	v_pk_mul_f32 v[100:101], v[214:215], v[100:101] op_sel_hi:[0,1]
	v_pk_mul_f32 v[102:103], v[214:215], v[102:103] op_sel_hi:[0,1]
	v_pk_fma_f32 v[96:97], v[44:45], v[96:97], v[122:123]
	v_pk_fma_f32 v[98:99], v[46:47], v[98:99], v[104:105]
	v_pk_fma_f32 v[100:101], v[36:37], v[100:101], v[128:129]
	v_pk_fma_f32 v[102:103], v[38:39], v[102:103], v[106:107]
	global_store_dwordx4 v[124:125], v[96:99], off offset:128
	global_store_dwordx4 v[124:125], v[100:103], off offset:144
	v_lshl_add_u64 v[106:107], s[40:41], 0, v[118:119]
	global_load_dwordx4 v[224:227], v[230:231], off offset:64
	global_load_dwordx4 v[232:235], v[238:239], off offset:64
	v_lshl_add_u64 v[96:97], v[114:115], 2, s[34:35]
	v_add_f32_e32 v108, 1.0, v89
	v_add_f32_e32 v97, 1.0, v88
	v_add_f32_e32 v109, 1.0, v90
	v_add_f32_e32 v110, 1.0, v91
	v_rcp_f32_e32 v88, v92
	v_rcp_f32_e32 v89, v93
	v_rcp_f32_e32 v90, v94
	v_rcp_f32_e32 v91, v95
	v_rcp_f32_e32 v92, v97
	v_rcp_f32_e32 v93, v108
	v_rcp_f32_e32 v94, v109
	v_rcp_f32_e32 v95, v110
	v_lshl_add_u64 v[108:109], v[116:117], 2, s[28:29]
	s_waitcnt vmcnt(6)
	v_lshlrev_b32_e32 v112, 16, v220
	v_and_b32_e32 v113, 0xffff0000, v220
	v_lshlrev_b32_e32 v102, 16, v221
	v_and_b32_e32 v103, 0xffff0000, v221
	v_lshlrev_b32_e32 v116, 16, v222
	v_and_b32_e32 v117, 0xffff0000, v222
	v_lshlrev_b32_e32 v104, 16, v223
	v_and_b32_e32 v105, 0xffff0000, v223
	v_pk_mul_f32 v[88:89], v[88:89], v[112:113]
	v_pk_mul_f32 v[90:91], v[90:91], v[102:103]
	s_waitcnt vmcnt(5)
	v_lshlrev_b32_e32 v110, 16, v216
	v_and_b32_e32 v111, 0xffff0000, v216
	v_lshlrev_b32_e32 v98, 16, v217
	v_and_b32_e32 v99, 0xffff0000, v217
	v_pk_mul_f32 v[92:93], v[92:93], v[116:117]
	v_pk_mul_f32 v[94:95], v[94:95], v[104:105]
	s_waitcnt vmcnt(4)
	v_pk_mul_f32 v[88:89], v[228:229], v[88:89] op_sel_hi:[0,1]
	v_pk_mul_f32 v[90:91], v[228:229], v[90:91] op_sel_hi:[0,1]
	v_lshlrev_b32_e32 v114, 16, v218
	v_and_b32_e32 v115, 0xffff0000, v218
	v_lshlrev_b32_e32 v100, 16, v219
	v_and_b32_e32 v101, 0xffff0000, v219
	v_pk_mul_f32 v[92:93], v[228:229], v[92:93] op_sel_hi:[0,1]
	v_pk_mul_f32 v[94:95], v[228:229], v[94:95] op_sel_hi:[0,1]
	v_pk_fma_f32 v[88:89], v[52:53], v[88:89], v[110:111]
	v_pk_fma_f32 v[90:91], v[54:55], v[90:91], v[98:99]
	v_pk_fma_f32 v[92:93], v[48:49], v[92:93], v[114:115]
	v_pk_fma_f32 v[94:95], v[50:51], v[94:95], v[100:101]
	global_store_dwordx4 v[108:109], v[88:91], off
	global_store_dwordx4 v[108:109], v[92:95], off offset:16
	v_lshl_add_u64 v[238:239], v[238:239], 0, s[100:101]
	global_load_dwordx4 v[220:223], v[238:239], off
	v_lshl_add_u64 v[230:231], v[230:231], 0, s[100:101]
	global_load_dwordx4 v[216:219], v[230:231], off
	global_load_dword v214, v[236:237], off offset:384
	s_nop 0
	v_add_f32_e32 v97, 1.0, v80
	v_add_f32_e32 v100, 1.0, v81
	v_add_f32_e32 v101, 1.0, v82
	v_add_f32_e32 v102, 1.0, v83
	v_rcp_f32_e32 v80, v84
	v_rcp_f32_e32 v81, v85
	v_rcp_f32_e32 v82, v86
	v_rcp_f32_e32 v83, v87
	v_rcp_f32_e32 v84, v97
	v_rcp_f32_e32 v85, v100
	v_rcp_f32_e32 v86, v101
	v_rcp_f32_e32 v87, v102
	v_add_u32_e32 v98, 0x60, v170
	v_ashrrev_i32_e32 v99, 31, v98
	v_lshlrev_b64 v[100:101], 11, v[98:99]
	v_lshl_add_u64 v[100:101], v[100:101], 0, v[168:169]
	v_lshlrev_b64 v[102:103], 1, v[100:101]
	v_lshl_add_u64 v[104:105], s[30:31], 0, v[102:103]
	s_waitcnt vmcnt(6)
	v_lshlrev_b32_e32 v106, 16, v224
	s_waitcnt vmcnt(5)
	v_lshlrev_b32_e32 v110, 16, v232
	v_and_b32_e32 v111, 0xffff0000, v232
	v_lshlrev_b32_e32 v92, 16, v233
	v_and_b32_e32 v93, 0xffff0000, v233
	v_lshlrev_b32_e32 v114, 16, v234
	v_and_b32_e32 v115, 0xffff0000, v234
	v_lshlrev_b32_e32 v94, 16, v235
	v_and_b32_e32 v95, 0xffff0000, v235
	v_pk_mul_f32 v[80:81], v[80:81], v[110:111]
	v_pk_mul_f32 v[82:83], v[82:83], v[92:93]
	v_and_b32_e32 v107, 0xffff0000, v224
	v_lshlrev_b32_e32 v88, 16, v225
	v_and_b32_e32 v89, 0xffff0000, v225
	v_pk_mul_f32 v[84:85], v[84:85], v[114:115]
	v_pk_mul_f32 v[86:87], v[86:87], v[94:95]
	v_pk_mul_f32 v[80:81], v[228:229], v[80:81] op_sel_hi:[0,1]
	v_pk_mul_f32 v[82:83], v[228:229], v[82:83] op_sel_hi:[0,1]
	v_lshlrev_b32_e32 v112, 16, v226
	v_and_b32_e32 v113, 0xffff0000, v226
	v_lshlrev_b32_e32 v90, 16, v227
	v_and_b32_e32 v91, 0xffff0000, v227
	v_pk_mul_f32 v[84:85], v[228:229], v[84:85] op_sel_hi:[0,1]
	v_pk_mul_f32 v[86:87], v[228:229], v[86:87] op_sel_hi:[0,1]
	v_pk_fma_f32 v[80:81], v[44:45], v[80:81], v[106:107]
	v_pk_fma_f32 v[82:83], v[46:47], v[82:83], v[88:89]
	v_pk_fma_f32 v[84:85], v[36:37], v[84:85], v[112:113]
	v_pk_fma_f32 v[86:87], v[38:39], v[86:87], v[90:91]
	global_store_dwordx4 v[108:109], v[80:83], off offset:128
	global_store_dwordx4 v[108:109], v[84:87], off offset:144
	v_lshl_add_u64 v[90:91], s[40:41], 0, v[102:103]
	global_load_dwordx4 v[224:227], v[230:231], off offset:64
	global_load_dwordx4 v[232:235], v[238:239], off offset:64
	v_lshl_add_u64 v[80:81], v[98:99], 2, s[34:35]
	v_add_f32_e32 v92, 1.0, v73
	v_add_f32_e32 v81, 1.0, v72
	v_add_f32_e32 v93, 1.0, v74
	v_add_f32_e32 v94, 1.0, v75
	v_rcp_f32_e32 v72, v76
	v_rcp_f32_e32 v73, v77
	v_rcp_f32_e32 v74, v78
	v_rcp_f32_e32 v75, v79
	v_rcp_f32_e32 v76, v81
	v_rcp_f32_e32 v77, v92
	v_rcp_f32_e32 v78, v93
	v_rcp_f32_e32 v79, v94
	v_lshl_add_u64 v[92:93], v[100:101], 2, s[28:29]
	s_waitcnt vmcnt(6)
	v_lshlrev_b32_e32 v96, 16, v220
	v_and_b32_e32 v97, 0xffff0000, v220
	v_lshlrev_b32_e32 v86, 16, v221
	v_and_b32_e32 v87, 0xffff0000, v221
	v_lshlrev_b32_e32 v100, 16, v222
	v_and_b32_e32 v101, 0xffff0000, v222
	v_lshlrev_b32_e32 v88, 16, v223
	v_and_b32_e32 v89, 0xffff0000, v223
	v_pk_mul_f32 v[72:73], v[72:73], v[96:97]
	v_pk_mul_f32 v[74:75], v[74:75], v[86:87]
	s_waitcnt vmcnt(5)
	v_lshlrev_b32_e32 v94, 16, v216
	v_and_b32_e32 v95, 0xffff0000, v216
	v_lshlrev_b32_e32 v82, 16, v217
	v_and_b32_e32 v83, 0xffff0000, v217
	v_pk_mul_f32 v[76:77], v[76:77], v[100:101]
	v_pk_mul_f32 v[78:79], v[78:79], v[88:89]
	s_waitcnt vmcnt(4)
	v_pk_mul_f32 v[72:73], v[214:215], v[72:73] op_sel_hi:[0,1]
	v_pk_mul_f32 v[74:75], v[214:215], v[74:75] op_sel_hi:[0,1]
	v_lshlrev_b32_e32 v98, 16, v218
	v_and_b32_e32 v99, 0xffff0000, v218
	v_lshlrev_b32_e32 v84, 16, v219
	v_and_b32_e32 v85, 0xffff0000, v219
	v_pk_mul_f32 v[76:77], v[214:215], v[76:77] op_sel_hi:[0,1]
	v_pk_mul_f32 v[78:79], v[214:215], v[78:79] op_sel_hi:[0,1]
	v_pk_fma_f32 v[72:73], v[52:53], v[72:73], v[94:95]
	v_pk_fma_f32 v[74:75], v[54:55], v[74:75], v[82:83]
	v_pk_fma_f32 v[76:77], v[48:49], v[76:77], v[98:99]
	v_pk_fma_f32 v[78:79], v[50:51], v[78:79], v[84:85]
	global_store_dwordx4 v[92:93], v[72:75], off
	global_store_dwordx4 v[92:93], v[76:79], off offset:16
	v_lshl_add_u64 v[238:239], v[238:239], 0, s[100:101]
	global_load_dwordx4 v[220:223], v[238:239], off
	v_lshl_add_u64 v[230:231], v[230:231], 0, s[100:101]
	global_load_dwordx4 v[216:219], v[230:231], off
	global_load_dword v228, v[236:237], off offset:448
	s_nop 0
	v_add_f32_e32 v81, 1.0, v64
	v_add_f32_e32 v84, 1.0, v65
	v_add_f32_e32 v85, 1.0, v66
	v_add_f32_e32 v86, 1.0, v67
	v_rcp_f32_e32 v64, v68
	v_rcp_f32_e32 v65, v69
	v_rcp_f32_e32 v66, v70
	v_rcp_f32_e32 v67, v71
	v_rcp_f32_e32 v68, v81
	v_rcp_f32_e32 v69, v84
	v_rcp_f32_e32 v70, v85
	v_rcp_f32_e32 v71, v86
	v_add_u32_e32 v82, 0x70, v170
	v_ashrrev_i32_e32 v83, 31, v82
	v_lshlrev_b64 v[84:85], 11, v[82:83]
	v_lshl_add_u64 v[84:85], v[84:85], 0, v[168:169]
	v_lshlrev_b64 v[86:87], 1, v[84:85]
	v_lshl_add_u64 v[88:89], s[30:31], 0, v[86:87]
	s_waitcnt vmcnt(6)
	v_lshlrev_b32_e32 v90, 16, v224
	s_waitcnt vmcnt(5)
	v_lshlrev_b32_e32 v94, 16, v232
	v_and_b32_e32 v95, 0xffff0000, v232
	v_lshlrev_b32_e32 v76, 16, v233
	v_and_b32_e32 v77, 0xffff0000, v233
	v_lshlrev_b32_e32 v98, 16, v234
	v_and_b32_e32 v99, 0xffff0000, v234
	v_lshlrev_b32_e32 v78, 16, v235
	v_and_b32_e32 v79, 0xffff0000, v235
	v_pk_mul_f32 v[64:65], v[64:65], v[94:95]
	v_pk_mul_f32 v[66:67], v[66:67], v[76:77]
	v_and_b32_e32 v91, 0xffff0000, v224
	v_lshlrev_b32_e32 v72, 16, v225
	v_and_b32_e32 v73, 0xffff0000, v225
	v_pk_mul_f32 v[68:69], v[68:69], v[98:99]
	v_pk_mul_f32 v[70:71], v[70:71], v[78:79]
	v_pk_mul_f32 v[64:65], v[214:215], v[64:65] op_sel_hi:[0,1]
	v_pk_mul_f32 v[66:67], v[214:215], v[66:67] op_sel_hi:[0,1]
	v_lshlrev_b32_e32 v96, 16, v226
	v_and_b32_e32 v97, 0xffff0000, v226
	v_lshlrev_b32_e32 v74, 16, v227
	v_and_b32_e32 v75, 0xffff0000, v227
	v_pk_mul_f32 v[68:69], v[214:215], v[68:69] op_sel_hi:[0,1]
	v_pk_mul_f32 v[70:71], v[214:215], v[70:71] op_sel_hi:[0,1]
	v_pk_fma_f32 v[64:65], v[44:45], v[64:65], v[90:91]
	v_pk_fma_f32 v[66:67], v[46:47], v[66:67], v[72:73]
	v_pk_fma_f32 v[68:69], v[36:37], v[68:69], v[96:97]
	v_pk_fma_f32 v[70:71], v[38:39], v[70:71], v[74:75]
	global_store_dwordx4 v[92:93], v[64:67], off offset:128
	global_store_dwordx4 v[92:93], v[68:71], off offset:144
	v_lshl_add_u64 v[74:75], s[40:41], 0, v[86:87]
	global_load_dwordx4 v[224:227], v[230:231], off offset:64
	global_load_dwordx4 v[232:235], v[238:239], off offset:64
	v_lshl_add_u64 v[64:65], v[82:83], 2, s[34:35]
	v_add_f32_e32 v76, 1.0, v57
	v_add_f32_e32 v65, 1.0, v56
	v_add_f32_e32 v77, 1.0, v58
	v_add_f32_e32 v78, 1.0, v59
	v_rcp_f32_e32 v56, v60
	v_rcp_f32_e32 v57, v61
	v_rcp_f32_e32 v58, v62
	v_rcp_f32_e32 v59, v63
	v_rcp_f32_e32 v60, v65
	v_rcp_f32_e32 v61, v76
	v_rcp_f32_e32 v62, v77
	v_rcp_f32_e32 v63, v78
	v_lshl_add_u64 v[76:77], v[84:85], 2, s[28:29]
	s_waitcnt vmcnt(6)
	v_lshlrev_b32_e32 v80, 16, v220
	v_and_b32_e32 v81, 0xffff0000, v220
	v_lshlrev_b32_e32 v70, 16, v221
	v_and_b32_e32 v71, 0xffff0000, v221
	v_lshlrev_b32_e32 v84, 16, v222
	v_and_b32_e32 v85, 0xffff0000, v222
	v_lshlrev_b32_e32 v72, 16, v223
	v_and_b32_e32 v73, 0xffff0000, v223
	v_pk_mul_f32 v[56:57], v[56:57], v[80:81]
	v_pk_mul_f32 v[58:59], v[58:59], v[70:71]
	s_waitcnt vmcnt(5)
	v_lshlrev_b32_e32 v78, 16, v216
	v_and_b32_e32 v79, 0xffff0000, v216
	v_lshlrev_b32_e32 v66, 16, v217
	v_and_b32_e32 v67, 0xffff0000, v217
	v_pk_mul_f32 v[60:61], v[60:61], v[84:85]
	v_pk_mul_f32 v[62:63], v[62:63], v[72:73]
	s_waitcnt vmcnt(4)
	v_pk_mul_f32 v[56:57], v[228:229], v[56:57] op_sel_hi:[0,1]
	v_pk_mul_f32 v[58:59], v[228:229], v[58:59] op_sel_hi:[0,1]
	v_lshlrev_b32_e32 v82, 16, v218
	v_and_b32_e32 v83, 0xffff0000, v218
	v_lshlrev_b32_e32 v68, 16, v219
	v_and_b32_e32 v69, 0xffff0000, v219
	v_pk_mul_f32 v[60:61], v[228:229], v[60:61] op_sel_hi:[0,1]
	v_pk_mul_f32 v[62:63], v[228:229], v[62:63] op_sel_hi:[0,1]
	v_pk_fma_f32 v[52:53], v[52:53], v[56:57], v[78:79]
	v_pk_fma_f32 v[54:55], v[54:55], v[58:59], v[66:67]
	v_pk_fma_f32 v[48:49], v[48:49], v[60:61], v[82:83]
	v_pk_fma_f32 v[50:51], v[50:51], v[62:63], v[68:69]
	global_store_dwordx4 v[76:77], v[52:55], off
	global_store_dwordx4 v[76:77], v[48:51], off offset:16
	s_nop 0
	v_add_f32_e32 v56, 1.0, v32
	v_add_f32_e32 v57, 1.0, v33
	v_add_f32_e32 v58, 1.0, v34
	v_add_f32_e32 v59, 1.0, v35
	v_rcp_f32_e32 v32, v40
	v_rcp_f32_e32 v33, v41
	v_rcp_f32_e32 v34, v42
	v_rcp_f32_e32 v35, v43
	v_rcp_f32_e32 v40, v56
	v_rcp_f32_e32 v41, v57
	v_rcp_f32_e32 v42, v58
	v_rcp_f32_e32 v43, v59
	s_waitcnt vmcnt(3)
	v_lshlrev_b32_e32 v56, 16, v224
	s_waitcnt vmcnt(2)
	v_lshlrev_b32_e32 v58, 16, v232
	v_and_b32_e32 v59, 0xffff0000, v232
	v_lshlrev_b32_e32 v52, 16, v233
	v_and_b32_e32 v53, 0xffff0000, v233
	v_lshlrev_b32_e32 v62, 16, v234
	v_and_b32_e32 v63, 0xffff0000, v234
	v_lshlrev_b32_e32 v54, 16, v235
	v_and_b32_e32 v55, 0xffff0000, v235
	v_pk_mul_f32 v[32:33], v[32:33], v[58:59]
	v_pk_mul_f32 v[34:35], v[34:35], v[52:53]
	v_and_b32_e32 v57, 0xffff0000, v224
	v_lshlrev_b32_e32 v48, 16, v225
	v_and_b32_e32 v49, 0xffff0000, v225
	v_pk_mul_f32 v[40:41], v[40:41], v[62:63]
	v_pk_mul_f32 v[42:43], v[42:43], v[54:55]
	v_pk_mul_f32 v[32:33], v[228:229], v[32:33] op_sel_hi:[0,1]
	v_pk_mul_f32 v[34:35], v[228:229], v[34:35] op_sel_hi:[0,1]
	v_lshlrev_b32_e32 v60, 16, v226
	v_and_b32_e32 v61, 0xffff0000, v226
	v_lshlrev_b32_e32 v50, 16, v227
	v_and_b32_e32 v51, 0xffff0000, v227
	v_pk_mul_f32 v[40:41], v[228:229], v[40:41] op_sel_hi:[0,1]
	v_pk_mul_f32 v[42:43], v[228:229], v[42:43] op_sel_hi:[0,1]
	v_pk_fma_f32 v[32:33], v[44:45], v[32:33], v[56:57]
	v_pk_fma_f32 v[34:35], v[46:47], v[34:35], v[48:49]
	v_pk_fma_f32 v[36:37], v[36:37], v[40:41], v[60:61]
	v_pk_fma_f32 v[38:39], v[38:39], v[42:43], v[50:51]
	global_store_dwordx4 v[76:77], v[32:35], off offset:128
	global_store_dwordx4 v[76:77], v[36:39], off offset:144
	s_cbranch_vccnz .LBB0_1042
